# per-tile scheduler step made branch-free and interleaved between the MFMAs of the peeled first K-iteration (4 GEMM instances)
# baseline (speedup 1.0000x reference)
; #define PG8_STAGE(bufoff, gbase, voff) do { _Pragma("unroll") for (int _i = 0; _i < 2; ++_i) \
;         __builtin_amdgcn_global_load_lds((const unsigned*)((const char*)(gbase) + (voff)[_i]), (PG8_LAS unsigned*)(lds + (bufoff) + ldsw + _i * 8192), 16, 0, 0); } while (0)
; #define PG8_LDA(dst, b, h) do { _Pragma("unroll") for (int m = 0; m < 4; ++m) _Pragma("unroll") for (int k = 0; k < 2; ++k) dst[m][k] = *(const PG8_LAS bf16x8*)(lds + PG8_SA(b, h) + aoff + m * 2048 + k * 1024); } while (0)
; #define PG8_LDB(dst, b, h) do { _Pragma("unroll") for (int n = 0; n < 2; ++n) _Pragma("unroll") for (int k = 0; k < 2; ++k) dst[n][k] = *(const PG8_LAS bf16x8*)(lds + PG8_SB(b, h) + boff + n * 2048 + k * 1024); } while (0)
; #define PG8_BAR __builtin_amdgcn_s_barrier()
;     __host__ __device__ bool next(int i, Unit& u) const {
;         const long L = (long)i * G + c; if (L >= nwg) return false;
;         int wgid = (int)L; { const int q = nwg / NXCD, r = nwg % NXCD, xcd = wgid % NXCD, off = wgid / NXCD; wgid = (xcd < r ? xcd * (q + 1) : r * (q + 1) + (xcd - r) * q) + off; }
;         const int nig = WGM * nN, gid = wgid / nig, fm = gid * WGM, gsz = (nM - fm) < WGM ? (nM - fm) : WGM;
;         u.pm = fm + ((wgid % nig) % gsz); u.pn = (wgid % nig) / gsz; return true;
;     }
; template <class Epi, class Sched, bool ALIGN_EPI = false, bool SP2 = false>
; __device__ __forceinline__ void gemm_phase(PG8_LAS unsigned char* lds, const Gemm g, const Sched& S, const Epi& E) {
;     ...
;         const bool has_next = S.next(ui + 1, nxt);
;         const char* nA = has_next ? (const char*)g.A + (size_t)nxt.pm * tstep : cA; const char* nB = has_next ? (const char*)g.Bt + (size_t)nxt.pn * tstep : cB;
;         for (int t = 0; t < nt; t += 2) {
;             const bool last = (t == nt - 2);
;             const char* a1 = cA + (size_t)(t + 1) * kstep;
;             const char* a2 = last ? nA : cA + (size_t)(t + 2) * kstep; const char* b2 = last ? nB : cB + (size_t)(t + 2) * kstep;
;             const char* a3 = a2 + kstep; const char* b3 = b2 + kstep;
;             if (last && has_next) S.a_ready(nxt);
;             if constexpr (SP2) {
;             PG8_LDB(B0, 0, 0); PG8_LDB(B1, 0, 1); PG8_SCHED; PG8_LDA(At, 0, 0); PG8_STAGE(PG8_SA(1, 1), a1 + hstep, voffA);
;             PG8_WAIT_V(8); PG8_WAIT_L(0); PG8_BAR; PG8_MMA(0, 0, At, B0); PG8_MMA(0, 1, At, B1); PG8_BAR; PG8_SCHED;
.LBB0_364:
	s_add_u32 s30, s30, 0x80080
	s_addc_u32 s31, s31, 0
	s_add_u32 s56, s34, 0x100
	s_addc_u32 s57, s35, 0
	s_mov_b32 s58, -2
	v_add_u32_e32 v248, 0x18000, v154
	v_add_u32_e32 v249, 0x1c000, v154
	ds_read_b128 v[148:151], v156
	ds_read_b128 v[160:163], v156 offset:1024
	ds_read_b128 v[164:167], v156 offset:2048
	ds_read_b128 v[168:171], v156 offset:3072
	ds_read_b128 v[172:175], v157
	ds_read_b128 v[176:179], v157 offset:1024
	ds_read_b128 v[180:183], v157 offset:2048
	ds_read_b128 v[188:191], v157 offset:3072
	s_add_u32 s34, s30, 0xfff80080
	s_addc_u32 s35, s31, -1
	s_cmp_eq_u32 s58, 28
	s_cselect_b32 s37, s23, s35
	s_cselect_b32 s36, s29, s34
	s_cselect_b32 s35, s21, s57
	s_cselect_b32 s34, s55, s56
	s_add_i32 m0, s42, 0xc000
	ds_read_b128 v[192:195], v158
	ds_read_b128 v[196:199], v158 offset:1024
	ds_read_b128 v[200:203], v158 offset:2048
	ds_read_b128 v[204:207], v158 offset:3072
	ds_read_b128 v[212:215], v158 offset:4096
	ds_read_b128 v[216:219], v158 offset:5120
	ds_read_b128 v[220:223], v158 offset:6144
	ds_read_b128 v[224:227], v158 offset:7168
	global_load_lds_dwordx4 v140, s[30:31]
	s_add_i32 m0, s42, 0xe000
	s_nop 0
	global_load_lds_dwordx4 v142, s[30:31]
	s_waitcnt vmcnt(8)
	s_waitcnt lgkmcnt(0)
	s_barrier
	s_setprio 1
	s_waitcnt lgkmcnt(0)
	v_mfma_f32_16x16x32_bf16 v[126:129], v[148:151], v[192:195], 0
	s_add_i32 s46, s46, 1
	s_mul_i32 s2, s46, s50
	s_mul_hi_u32 s3, s46, s82
	v_mfma_f32_16x16x32_bf16 v[122:125], v[164:167], v[192:195], 0
	s_add_i32 s3, s3, s2
	s_mul_i32 s2, s46, s82
	v_readlane_b32 s21, v247, 6
	v_mfma_f32_16x16x32_bf16 v[118:121], v[148:151], v[200:203], 0
	s_add_u32 s24, s2, s21
	s_addc_u32 s25, s3, s40
	v_cmp_lt_i64_e64 s[2:3], s[24:25], v[144:145]
	v_mfma_f32_16x16x32_bf16 v[110:113], v[164:167], v[200:203], 0
	s_ashr_i32 s20, s24, 31
	s_lshr_b32 s20, s20, 29
	s_add_i32 s20, s24, s20
	v_mfma_f32_16x16x32_bf16 v[102:105], v[148:151], v[212:215], 0
	s_ashr_i32 s21, s20, 3
	s_and_b32 s20, s20, -8
	s_sub_i32 s20, s24, s20
	v_mfma_f32_16x16x32_bf16 v[94:97], v[164:167], v[212:215], 0
	s_cmp_lt_i32 s20, 0
	s_cselect_b32 s22, s41, 0x90
	s_mul_i32 s20, s20, s22
	v_mfma_f32_16x16x32_bf16 v[86:89], v[148:151], v[220:223], 0
	s_add_i32 s20, s20, s21
	s_mul_hi_i32 s21, s20, 0x38e38e39
	s_lshr_b32 s22, s21, 31
	v_mfma_f32_16x16x32_bf16 v[78:81], v[164:167], v[220:223], 0
	s_ashr_i32 s21, s21, 5
	s_add_i32 s21, s21, s22
	s_lshl_b32 s22, s21, 3
	v_mfma_f32_16x16x32_bf16 v[126:129], v[160:163], v[196:199], v[126:129]
	s_sub_i32 s23, 64, s22
	s_min_i32 s23, s23, 8
	s_abs_i32 s24, s23
	v_mfma_f32_16x16x32_bf16 v[122:125], v[168:171], v[196:199], v[122:125]
	v_cvt_f32_u32_e32 v250, s24
	s_sub_i32 s26, 0, s24
	s_mulk_i32 s21, 0x90
	v_mfma_f32_16x16x32_bf16 v[118:121], v[160:163], v[204:207], v[118:121]
	s_sub_i32 s21, s20, s21
	v_rcp_iflag_f32_e32 v250, v250
	s_abs_i32 s20, s21
	v_mfma_f32_16x16x32_bf16 v[110:113], v[168:171], v[204:207], v[110:113]
	s_xor_b32 s25, s21, s23
	s_ashr_i32 s25, s25, 31
	v_mul_f32_e32 v250, 0x4f7ffffe, v250
	v_mfma_f32_16x16x32_bf16 v[102:105], v[160:163], v[216:219], v[102:105]
	v_cvt_u32_f32_e32 v250, v250
	s_nop 0
	v_readfirstlane_b32 s27, v250
	v_mfma_f32_16x16x32_bf16 v[94:97], v[168:171], v[216:219], v[94:97]
	s_mul_i32 s26, s26, s27
	s_mul_hi_u32 s26, s27, s26
	s_add_i32 s27, s27, s26
	v_mfma_f32_16x16x32_bf16 v[86:89], v[160:163], v[224:227], v[86:89]
	s_mul_hi_u32 s26, s20, s27
	s_mul_i32 s27, s26, s24
	s_sub_i32 s20, s20, s27
	v_mfma_f32_16x16x32_bf16 v[78:81], v[168:171], v[224:227], v[78:81]
	s_add_i32 s29, s26, 1
	s_sub_i32 s27, s20, s24
	s_cmp_ge_u32 s20, s24
	s_setprio 0
	s_setprio 1
	v_mfma_f32_16x16x32_bf16 v[114:117], v[172:175], v[192:195], 0
	s_cselect_b32 s26, s29, s26
	s_cselect_b32 s20, s27, s20
	s_add_i32 s27, s26, 1
	v_mfma_f32_16x16x32_bf16 v[106:109], v[180:183], v[192:195], 0
	s_cmp_ge_u32 s20, s24
	s_cselect_b32 s20, s27, s26
	s_xor_b32 s20, s20, s25
	v_mfma_f32_16x16x32_bf16 v[98:101], v[172:175], v[200:203], 0
	s_sub_i32 s20, s20, s25
	s_mul_i32 s23, s20, s23
	s_sub_i32 s21, s21, s23
	v_mfma_f32_16x16x32_bf16 v[90:93], v[180:183], v[200:203], 0
	s_add_i32 s22, s22, s21
	s_ashr_i32 s23, s22, 31
	s_lshl_b64 s[24:25], s[22:23], 20
	v_mfma_f32_16x16x32_bf16 v[82:85], v[172:175], v[212:215], 0
	s_add_u32 s24, s70, s24
	s_addc_u32 s25, s71, s25
	s_and_b64 s[26:27], s[2:3], exec
	v_mfma_f32_16x16x32_bf16 v[74:77], v[180:183], v[212:215], 0
	s_cselect_b32 s23, s25, s31
	s_cselect_b32 s29, s24, s30
	s_ashr_i32 s21, s20, 31
	v_mfma_f32_16x16x32_bf16 v[70:73], v[172:175], v[220:223], 0
	s_lshl_b64 s[26:27], s[20:21], 20
	s_add_u32 s26, s33, s26
	s_addc_u32 s27, s38, s27
	v_mfma_f32_16x16x32_bf16 v[66:69], v[180:183], v[220:223], 0
	s_and_b64 s[98:99], s[2:3], exec
	s_cselect_b32 s21, s27, s35
	s_cselect_b32 s55, s26, s34
	v_mfma_f32_16x16x32_bf16 v[114:117], v[176:179], v[196:199], v[114:117]
	v_mfma_f32_16x16x32_bf16 v[106:109], v[188:191], v[196:199], v[106:109]
	v_mfma_f32_16x16x32_bf16 v[98:101], v[176:179], v[204:207], v[98:101]
	v_mfma_f32_16x16x32_bf16 v[90:93], v[188:191], v[204:207], v[90:93]
	v_mfma_f32_16x16x32_bf16 v[82:85], v[176:179], v[216:219], v[82:85]
	v_mfma_f32_16x16x32_bf16 v[74:77], v[188:191], v[216:219], v[74:77]
	v_mfma_f32_16x16x32_bf16 v[70:73], v[176:179], v[224:227], v[70:73]
	v_mfma_f32_16x16x32_bf16 v[66:69], v[188:191], v[224:227], v[66:69]
	s_setprio 0
	s_barrier
; #define PG8_STAGE(bufoff, gbase, voff) do { _Pragma("unroll") for (int _i = 0; _i < 2; ++_i) \
;         __builtin_amdgcn_global_load_lds((const unsigned*)((const char*)(gbase) + (voff)[_i]), (PG8_LAS unsigned*)(lds + (bufoff) + ldsw + _i * 8192), 16, 0, 0); } while (0)
; #define PG8_LDA(dst, b, h) do { _Pragma("unroll") for (int m = 0; m < 4; ++m) _Pragma("unroll") for (int k = 0; k < 2; ++k) dst[m][k] = *(const PG8_LAS bf16x8*)(lds + PG8_SA(b, h) + aoff + m * 2048 + k * 1024); } while (0)
; #define PG8_LDB(dst, b, h) do { _Pragma("unroll") for (int n = 0; n < 2; ++n) _Pragma("unroll") for (int k = 0; k < 2; ++k) dst[n][k] = *(const PG8_LAS bf16x8*)(lds + PG8_SB(b, h) + boff + n * 2048 + k * 1024); } while (0)
; #define PG8_WAIT_V(n) asm volatile("s_waitcnt vmcnt(" #n ")" ::: "memory")
; #define PG8_WAIT_L(n) asm volatile("s_waitcnt lgkmcnt(" #n ")" ::: "memory")
; #define PG8_BAR __builtin_amdgcn_s_barrier()
; #define PG8_SCHED __builtin_amdgcn_sched_barrier(0)
; template <class Epi, class Sched, bool ALIGN_EPI = false, bool SP2 = false>
; __device__ __forceinline__ void gemm_phase(PG8_LAS unsigned char* lds, const Gemm g, const Sched& S, const Epi& E) {
;     ...
;             PG8_LDA(At, 0, 1); PG8_STAGE(PG8_SB(0, 0), b2, voffB); PG8_STAGE(PG8_SB(0, 1), b2 + hstep, voffB); PG8_STAGE(PG8_SA(0, 0), a2, voffA);
;             PG8_WAIT_V(8); PG8_WAIT_L(0); PG8_BAR; PG8_MMA(1, 0, At, B0); PG8_MMA(1, 1, At, B1); PG8_BAR; PG8_SCHED;
;             PG8_LDB(B0, 1, 0); PG8_LDB(B1, 1, 1); PG8_SCHED; PG8_LDA(At, 1, 0); PG8_STAGE(PG8_SA(0, 1), a2 + hstep, voffA);
;             PG8_WAIT_V(8); PG8_WAIT_L(0); PG8_BAR; PG8_MMA(0, 0, At, B0); PG8_MMA(0, 1, At, B1); PG8_BAR; PG8_SCHED;
	s_add_i32 s59, s51, s39
	s_mov_b32 m0, s59
	ds_read_b128 v[192:195], v158 offset:16384
	ds_read_b128 v[196:199], v158 offset:17408
	ds_read_b128 v[200:203], v158 offset:18432
	ds_read_b128 v[204:207], v158 offset:19456
	ds_read_b128 v[212:215], v158 offset:20480
	ds_read_b128 v[216:219], v158 offset:21504
	ds_read_b128 v[220:223], v158 offset:22528
	ds_read_b128 v[224:227], v158 offset:23552
	global_load_lds_dwordx4 v134, s[34:35]
	s_add_i32 m0, s59, 0x2000
	s_add_u32 s60, s34, 0x80000
	s_addc_u32 s61, s35, 0
	s_add_i32 s59, s52, s39
	global_load_lds_dwordx4 v130, s[34:35]
	s_mov_b32 m0, s59
	s_nop 0
	global_load_lds_dwordx4 v134, s[60:61]
	s_add_i32 m0, s59, 0x2000
	s_nop 0
	global_load_lds_dwordx4 v130, s[60:61]
	s_mov_b32 m0, s42
	s_nop 0
	global_load_lds_dwordx4 v136, s[36:37]
	s_mov_b32 m0, s43
	s_nop 0
	global_load_lds_dwordx4 v132, s[36:37]
	s_waitcnt vmcnt(8)
	s_waitcnt lgkmcnt(0)
	s_barrier
	s_setprio 1
	s_waitcnt lgkmcnt(0)
	v_mfma_f32_16x16x32_bf16 v[62:65], v[148:151], v[192:195], 0
	v_mfma_f32_16x16x32_bf16 v[58:61], v[164:167], v[192:195], 0
	v_mfma_f32_16x16x32_bf16 v[54:57], v[148:151], v[200:203], 0
	v_mfma_f32_16x16x32_bf16 v[46:49], v[164:167], v[200:203], 0
	v_mfma_f32_16x16x32_bf16 v[38:41], v[148:151], v[212:215], 0
	v_mfma_f32_16x16x32_bf16 v[30:33], v[164:167], v[212:215], 0
	v_mfma_f32_16x16x32_bf16 v[22:25], v[148:151], v[220:223], 0
	v_mfma_f32_16x16x32_bf16 v[14:17], v[164:167], v[220:223], 0
	v_mfma_f32_16x16x32_bf16 v[62:65], v[160:163], v[196:199], v[62:65]
	v_mfma_f32_16x16x32_bf16 v[58:61], v[168:171], v[196:199], v[58:61]
	v_mfma_f32_16x16x32_bf16 v[54:57], v[160:163], v[204:207], v[54:57]
	v_mfma_f32_16x16x32_bf16 v[46:49], v[168:171], v[204:207], v[46:49]
	v_mfma_f32_16x16x32_bf16 v[38:41], v[160:163], v[216:219], v[38:41]
	v_mfma_f32_16x16x32_bf16 v[30:33], v[168:171], v[216:219], v[30:33]
	v_mfma_f32_16x16x32_bf16 v[22:25], v[160:163], v[224:227], v[22:25]
	v_mfma_f32_16x16x32_bf16 v[14:17], v[168:171], v[224:227], v[14:17]
	s_setprio 0
	s_setprio 1
	v_mfma_f32_16x16x32_bf16 v[50:53], v[172:175], v[192:195], 0
	v_mfma_f32_16x16x32_bf16 v[42:45], v[180:183], v[192:195], 0
	v_mfma_f32_16x16x32_bf16 v[34:37], v[172:175], v[200:203], 0
	v_mfma_f32_16x16x32_bf16 v[26:29], v[180:183], v[200:203], 0
	v_mfma_f32_16x16x32_bf16 v[18:21], v[172:175], v[212:215], 0
	v_mfma_f32_16x16x32_bf16 v[10:13], v[180:183], v[212:215], 0
	v_mfma_f32_16x16x32_bf16 v[6:9], v[172:175], v[220:223], 0
	v_mfma_f32_16x16x32_bf16 v[2:5], v[180:183], v[220:223], 0
	v_mfma_f32_16x16x32_bf16 v[50:53], v[176:179], v[196:199], v[50:53]
	v_mfma_f32_16x16x32_bf16 v[42:45], v[188:191], v[196:199], v[42:45]
	v_mfma_f32_16x16x32_bf16 v[34:37], v[176:179], v[204:207], v[34:37]
	v_mfma_f32_16x16x32_bf16 v[26:29], v[188:191], v[204:207], v[26:29]
	v_mfma_f32_16x16x32_bf16 v[18:21], v[176:179], v[216:219], v[18:21]
	v_mfma_f32_16x16x32_bf16 v[10:13], v[188:191], v[216:219], v[10:13]
	v_mfma_f32_16x16x32_bf16 v[6:9], v[176:179], v[224:227], v[6:9]
	v_mfma_f32_16x16x32_bf16 v[2:5], v[188:191], v[224:227], v[2:5]
	s_setprio 0
	s_barrier
	s_add_i32 s59, 0, 0x18000
	s_add_i32 s60, 0, 0x1c000
	ds_read_b128 v[148:151], v248
	ds_read_b128 v[160:163], v248 offset:1024
	ds_read_b128 v[164:167], v248 offset:2048
	ds_read_b128 v[168:171], v248 offset:3072
	ds_read_b128 v[172:175], v249
	ds_read_b128 v[176:179], v249 offset:1024
	ds_read_b128 v[180:183], v249 offset:2048
	ds_read_b128 v[188:191], v249 offset:3072
	s_add_u32 s36, s36, 0x80000
	s_addc_u32 s37, s37, 0
	s_mov_b32 m0, s44
	ds_read_b128 v[192:195], v158 offset:32768
	ds_read_b128 v[196:199], v158 offset:33792
	ds_read_b128 v[200:203], v158 offset:34816
	ds_read_b128 v[204:207], v158 offset:35840
	ds_read_b128 v[212:215], v158 offset:36864
	ds_read_b128 v[216:219], v158 offset:37888
	ds_read_b128 v[220:223], v158 offset:38912
	ds_read_b128 v[224:227], v158 offset:39936
	global_load_lds_dwordx4 v136, s[36:37]
	s_mov_b32 m0, s45
	s_nop 0
	global_load_lds_dwordx4 v132, s[36:37]
	s_waitcnt vmcnt(8)
	s_waitcnt lgkmcnt(0)
	s_barrier
; #define PG8_STAGE(bufoff, gbase, voff) do { _Pragma("unroll") for (int _i = 0; _i < 2; ++_i) \
;         __builtin_amdgcn_global_load_lds((const unsigned*)((const char*)(gbase) + (voff)[_i]), (PG8_LAS unsigned*)(lds + (bufoff) + ldsw + _i * 8192), 16, 0, 0); } while (0)
; #define PG8_LDA(dst, b, h) do { _Pragma("unroll") for (int m = 0; m < 4; ++m) _Pragma("unroll") for (int k = 0; k < 2; ++k) dst[m][k] = *(const PG8_LAS bf16x8*)(lds + PG8_SA(b, h) + aoff + m * 2048 + k * 1024); } while (0)
; #define PG8_WAIT_V(n) asm volatile("s_waitcnt vmcnt(" #n ")" ::: "memory")
; #define PG8_WAIT_L(n) asm volatile("s_waitcnt lgkmcnt(" #n ")" ::: "memory")
; #define PG8_BAR __builtin_amdgcn_s_barrier()
; #define PG8_SCHED __builtin_amdgcn_sched_barrier(0)
; template <class Epi, class Sched, bool ALIGN_EPI = false, bool SP2 = false>
; __device__ __forceinline__ void gemm_phase(PG8_LAS unsigned char* lds, const Gemm g, const Sched& S, const Epi& E) {
;     ...
;             PG8_WAIT_V(8); PG8_WAIT_L(0); PG8_BAR; PG8_MMA(0, 0, At, B0); PG8_MMA(0, 1, At, B1); PG8_BAR; PG8_SCHED;
;             PG8_LDA(At, 1, 1); PG8_STAGE(PG8_SB(1, 0), b3, voffB); PG8_STAGE(PG8_SB(1, 1), b3 + hstep, voffB); PG8_STAGE(PG8_SA(1, 0), a3, voffA);
;             PG8_WAIT_V(8); PG8_WAIT_L(0); PG8_BAR; PG8_MMA(1, 0, At, B0); PG8_MMA(1, 1, At, B1); PG8_BAR; PG8_SCHED;
	s_setprio 1
	s_waitcnt lgkmcnt(0)
	v_mfma_f32_16x16x32_bf16 v[126:129], v[148:151], v[192:195], v[126:129]
	v_mfma_f32_16x16x32_bf16 v[122:125], v[164:167], v[192:195], v[122:125]
	v_mfma_f32_16x16x32_bf16 v[118:121], v[148:151], v[200:203], v[118:121]
	v_mfma_f32_16x16x32_bf16 v[110:113], v[164:167], v[200:203], v[110:113]
	v_mfma_f32_16x16x32_bf16 v[102:105], v[148:151], v[212:215], v[102:105]
	v_mfma_f32_16x16x32_bf16 v[94:97], v[164:167], v[212:215], v[94:97]
	v_mfma_f32_16x16x32_bf16 v[86:89], v[148:151], v[220:223], v[86:89]
	v_mfma_f32_16x16x32_bf16 v[78:81], v[164:167], v[220:223], v[78:81]
	v_mfma_f32_16x16x32_bf16 v[126:129], v[160:163], v[196:199], v[126:129]
	v_mfma_f32_16x16x32_bf16 v[122:125], v[168:171], v[196:199], v[122:125]
	v_mfma_f32_16x16x32_bf16 v[118:121], v[160:163], v[204:207], v[118:121]
	v_mfma_f32_16x16x32_bf16 v[110:113], v[168:171], v[204:207], v[110:113]
	v_mfma_f32_16x16x32_bf16 v[102:105], v[160:163], v[216:219], v[102:105]
	v_mfma_f32_16x16x32_bf16 v[94:97], v[168:171], v[216:219], v[94:97]
	v_mfma_f32_16x16x32_bf16 v[86:89], v[160:163], v[224:227], v[86:89]
	v_mfma_f32_16x16x32_bf16 v[78:81], v[168:171], v[224:227], v[78:81]
	s_setprio 0
	s_setprio 1
	v_mfma_f32_16x16x32_bf16 v[114:117], v[172:175], v[192:195], v[114:117]
	v_mfma_f32_16x16x32_bf16 v[106:109], v[180:183], v[192:195], v[106:109]
	v_mfma_f32_16x16x32_bf16 v[98:101], v[172:175], v[200:203], v[98:101]
	v_mfma_f32_16x16x32_bf16 v[90:93], v[180:183], v[200:203], v[90:93]
	v_mfma_f32_16x16x32_bf16 v[82:85], v[172:175], v[212:215], v[82:85]
	v_mfma_f32_16x16x32_bf16 v[74:77], v[180:183], v[212:215], v[74:77]
	v_mfma_f32_16x16x32_bf16 v[70:73], v[172:175], v[220:223], v[70:73]
	v_mfma_f32_16x16x32_bf16 v[66:69], v[180:183], v[220:223], v[66:69]
	v_mfma_f32_16x16x32_bf16 v[114:117], v[176:179], v[196:199], v[114:117]
	v_mfma_f32_16x16x32_bf16 v[106:109], v[188:191], v[196:199], v[106:109]
	v_mfma_f32_16x16x32_bf16 v[98:101], v[176:179], v[204:207], v[98:101]
	v_mfma_f32_16x16x32_bf16 v[90:93], v[188:191], v[204:207], v[90:93]
	v_mfma_f32_16x16x32_bf16 v[82:85], v[176:179], v[216:219], v[82:85]
	v_mfma_f32_16x16x32_bf16 v[74:77], v[188:191], v[216:219], v[74:77]
	v_mfma_f32_16x16x32_bf16 v[70:73], v[176:179], v[224:227], v[70:73]
	v_mfma_f32_16x16x32_bf16 v[66:69], v[188:191], v[224:227], v[66:69]
	s_setprio 0
	s_barrier
	s_add_u32 s98, s34, 0x80
	s_addc_u32 s99, s35, 0
	s_add_u32 s100, s36, 0xfff80080
	s_addc_u32 s101, s37, -1
	s_add_i32 s36, s59, s39
	s_mov_b32 m0, s36
	ds_read_b128 v[192:195], v158 offset:49152
	ds_read_b128 v[196:199], v158 offset:50176
	ds_read_b128 v[200:203], v158 offset:51200
	ds_read_b128 v[204:207], v158 offset:52224
	ds_read_b128 v[212:215], v158 offset:53248
	ds_read_b128 v[216:219], v158 offset:54272
	ds_read_b128 v[220:223], v158 offset:55296
	ds_read_b128 v[224:227], v158 offset:56320
	global_load_lds_dwordx4 v134, s[98:99]
	s_add_i32 m0, s36, 0x2000
	s_add_u32 s34, s34, 0x80080
	s_addc_u32 s35, s35, 0
	s_add_i32 s36, s60, s39
	global_load_lds_dwordx4 v130, s[98:99]
	s_mov_b32 m0, s36
	s_nop 0
	global_load_lds_dwordx4 v134, s[34:35]
	s_add_i32 m0, s36, 0x2000
	s_nop 0
	global_load_lds_dwordx4 v130, s[34:35]
	s_mov_b32 m0, s48
	s_nop 0
	global_load_lds_dwordx4 v136, s[100:101]
	s_mov_b32 m0, s49
	s_nop 0
	global_load_lds_dwordx4 v132, s[100:101]
	s_waitcnt vmcnt(8)
	s_waitcnt lgkmcnt(0)
	s_barrier
	s_setprio 1
	s_waitcnt lgkmcnt(0)
	v_mfma_f32_16x16x32_bf16 v[62:65], v[148:151], v[192:195], v[62:65]
	v_mfma_f32_16x16x32_bf16 v[58:61], v[164:167], v[192:195], v[58:61]
	v_mfma_f32_16x16x32_bf16 v[54:57], v[148:151], v[200:203], v[54:57]
	v_mfma_f32_16x16x32_bf16 v[46:49], v[164:167], v[200:203], v[46:49]
	v_mfma_f32_16x16x32_bf16 v[38:41], v[148:151], v[212:215], v[38:41]
	v_mfma_f32_16x16x32_bf16 v[30:33], v[164:167], v[212:215], v[30:33]
	v_mfma_f32_16x16x32_bf16 v[22:25], v[148:151], v[220:223], v[22:25]
	v_mfma_f32_16x16x32_bf16 v[14:17], v[164:167], v[220:223], v[14:17]
	v_mfma_f32_16x16x32_bf16 v[62:65], v[160:163], v[196:199], v[62:65]
	v_mfma_f32_16x16x32_bf16 v[58:61], v[168:171], v[196:199], v[58:61]
	v_mfma_f32_16x16x32_bf16 v[54:57], v[160:163], v[204:207], v[54:57]
	v_mfma_f32_16x16x32_bf16 v[46:49], v[168:171], v[204:207], v[46:49]
	v_mfma_f32_16x16x32_bf16 v[38:41], v[160:163], v[216:219], v[38:41]
	v_mfma_f32_16x16x32_bf16 v[30:33], v[168:171], v[216:219], v[30:33]
	v_mfma_f32_16x16x32_bf16 v[22:25], v[160:163], v[224:227], v[22:25]
	v_mfma_f32_16x16x32_bf16 v[14:17], v[168:171], v[224:227], v[14:17]
	s_setprio 0
	s_setprio 1
	v_mfma_f32_16x16x32_bf16 v[50:53], v[172:175], v[192:195], v[50:53]
	v_mfma_f32_16x16x32_bf16 v[42:45], v[180:183], v[192:195], v[42:45]
	v_mfma_f32_16x16x32_bf16 v[34:37], v[172:175], v[200:203], v[34:37]
	v_mfma_f32_16x16x32_bf16 v[26:29], v[180:183], v[200:203], v[26:29]
	v_mfma_f32_16x16x32_bf16 v[18:21], v[172:175], v[212:215], v[18:21]
	v_mfma_f32_16x16x32_bf16 v[10:13], v[180:183], v[212:215], v[10:13]
	v_mfma_f32_16x16x32_bf16 v[6:9], v[172:175], v[220:223], v[6:9]
	v_mfma_f32_16x16x32_bf16 v[2:5], v[180:183], v[220:223], v[2:5]
	v_mfma_f32_16x16x32_bf16 v[50:53], v[176:179], v[196:199], v[50:53]
	v_mfma_f32_16x16x32_bf16 v[42:45], v[188:191], v[196:199], v[42:45]
	v_mfma_f32_16x16x32_bf16 v[34:37], v[176:179], v[204:207], v[34:37]
	v_mfma_f32_16x16x32_bf16 v[26:29], v[188:191], v[204:207], v[26:29]
	v_mfma_f32_16x16x32_bf16 v[18:21], v[176:179], v[216:219], v[18:21]
	v_mfma_f32_16x16x32_bf16 v[10:13], v[188:191], v[216:219], v[10:13]
	v_mfma_f32_16x16x32_bf16 v[6:9], v[176:179], v[224:227], v[6:9]
	v_mfma_f32_16x16x32_bf16 v[2:5], v[188:191], v[224:227], v[2:5]
	s_setprio 0
	s_barrier
	s_add_i32 s58, s58, 2
	s_add_u32 s30, s30, 0x100
	s_addc_u32 s31, s31, 0
	s_add_u32 s56, s56, 0x100
	s_addc_u32 s57, s57, 0
	s_cmp_gt_u32 s58, 29

; #define PG8_STAGE(bufoff, gbase, voff) do { _Pragma("unroll") for (int _i = 0; _i < 2; ++_i) \
;         __builtin_amdgcn_global_load_lds((const unsigned*)((const char*)(gbase) + (voff)[_i]), (PG8_LAS unsigned*)(lds + (bufoff) + ldsw + _i * 8192), 16, 0, 0); } while (0)
; #define PG8_LDA(dst, b, h) do { _Pragma("unroll") for (int m = 0; m < 4; ++m) _Pragma("unroll") for (int k = 0; k < 2; ++k) dst[m][k] = *(const PG8_LAS bf16x8*)(lds + PG8_SA(b, h) + aoff + m * 2048 + k * 1024); } while (0)
; #define PG8_LDB(dst, b, h) do { _Pragma("unroll") for (int n = 0; n < 2; ++n) _Pragma("unroll") for (int k = 0; k < 2; ++k) dst[n][k] = *(const PG8_LAS bf16x8*)(lds + PG8_SB(b, h) + boff + n * 2048 + k * 1024); } while (0)
; #define PG8_BAR __builtin_amdgcn_s_barrier()
;     __host__ __device__ bool next(int i, Unit& u) const {
;         const long L = (long)i * G + c; if (L >= nwg) return false;
;         int wgid = (int)L; { const int q = nwg / NXCD, r = nwg % NXCD, xcd = wgid % NXCD, off = wgid / NXCD; wgid = (xcd < r ? xcd * (q + 1) : r * (q + 1) + (xcd - r) * q) + off; }
;         const int nig = WGM * nN, gid = wgid / nig, fm = gid * WGM, gsz = (nM - fm) < WGM ? (nM - fm) : WGM;
;         u.pm = fm + ((wgid % nig) % gsz); u.pn = (wgid % nig) / gsz; return true;
;     }
; template <class Epi, class Sched, bool ALIGN_EPI = false, bool SP2 = false>
; __device__ __forceinline__ void gemm_phase(PG8_LAS unsigned char* lds, const Gemm g, const Sched& S, const Epi& E) {
;     ...
;         const bool has_next = S.next(ui + 1, nxt);
;         const char* nA = has_next ? (const char*)g.A + (size_t)nxt.pm * tstep : cA; const char* nB = has_next ? (const char*)g.Bt + (size_t)nxt.pn * tstep : cB;
;         for (int t = 0; t < nt; t += 2) {
;             const bool last = (t == nt - 2);
;             const char* a1 = cA + (size_t)(t + 1) * kstep;
;             const char* a2 = last ? nA : cA + (size_t)(t + 2) * kstep; const char* b2 = last ? nB : cB + (size_t)(t + 2) * kstep;
;             const char* a3 = a2 + kstep; const char* b3 = b2 + kstep;
;             if (last && has_next) S.a_ready(nxt);
;             if constexpr (SP2) {
;             PG8_LDB(B0, 0, 0); PG8_LDB(B1, 0, 1); PG8_SCHED; PG8_LDA(At, 0, 0); PG8_STAGE(PG8_SA(1, 1), a1 + hstep, voffA);
;             PG8_WAIT_V(8); PG8_WAIT_L(0); PG8_BAR; PG8_MMA(0, 0, At, B0); PG8_MMA(0, 1, At, B1); PG8_BAR; PG8_SCHED;
.LBB0_869:
	s_add_u32 s22, s22, 0x80080
	s_addc_u32 s23, s23, 0
	s_add_u32 s46, s24, 0x100
	s_addc_u32 s47, s25, 0
	s_mov_b32 s48, -2
	v_add_u32_e32 v248, 0x18000, v151
	v_add_u32_e32 v249, 0x1c000, v151
	ds_read_b128 v[146:149], v153
	ds_read_b128 v[156:159], v153 offset:1024
	ds_read_b128 v[160:163], v153 offset:2048
	ds_read_b128 v[164:167], v153 offset:3072
	ds_read_b128 v[168:171], v154
	ds_read_b128 v[172:175], v154 offset:1024
	ds_read_b128 v[176:179], v154 offset:2048
	ds_read_b128 v[180:183], v154 offset:3072
	s_add_u32 s24, s22, 0xfff80080
	s_addc_u32 s25, s23, -1
	s_cmp_eq_u32 s48, 28
	s_cselect_b32 s27, s15, s25
	s_cselect_b32 s26, s44, s24
	s_cselect_b32 s25, s13, s47
	s_cselect_b32 s24, s45, s46
	s_add_i32 m0, s21, 0xc000
	ds_read_b128 v[190:193], v155
	ds_read_b128 v[194:197], v155 offset:1024
	ds_read_b128 v[198:201], v155 offset:2048
	ds_read_b128 v[202:205], v155 offset:3072
	ds_read_b128 v[206:209], v155 offset:4096
	ds_read_b128 v[216:219], v155 offset:5120
	ds_read_b128 v[220:223], v155 offset:6144
	ds_read_b128 v[224:227], v155 offset:7168
	global_load_lds_dwordx4 v138, s[22:23]
	s_add_i32 m0, s21, 0xe000
	s_nop 0
	global_load_lds_dwordx4 v140, s[22:23]
	s_waitcnt vmcnt(8)
	s_waitcnt lgkmcnt(0)
	s_barrier
	s_setprio 1
	s_waitcnt lgkmcnt(0)
	v_mfma_f32_16x16x32_bf16 v[126:129], v[146:149], v[190:193], 0
	s_add_i32 s36, s36, 1
	s_mul_i32 s2, s36, s39
	s_mul_hi_u32 s3, s36, s82
	v_mfma_f32_16x16x32_bf16 v[122:125], v[160:163], v[190:193], 0
	s_add_i32 s3, s3, s2
	s_mul_i32 s2, s36, s82
	v_readlane_b32 s13, v247, 6
	v_mfma_f32_16x16x32_bf16 v[110:113], v[146:149], v[198:201], 0
	s_add_u32 s16, s2, s13
	s_addc_u32 s17, s3, s30
	v_cmp_lt_i64_e64 s[2:3], s[16:17], v[142:143]
	v_mfma_f32_16x16x32_bf16 v[106:109], v[160:163], v[198:201], 0
	s_ashr_i32 s12, s16, 31
	s_lshr_b32 s12, s12, 29
	s_add_i32 s12, s16, s12
	v_mfma_f32_16x16x32_bf16 v[94:97], v[146:149], v[206:209], 0
	s_ashr_i32 s13, s12, 3
	s_and_b32 s12, s12, -8
	s_sub_i32 s12, s16, s12
	v_mfma_f32_16x16x32_bf16 v[90:93], v[160:163], v[206:209], 0
	s_cmp_lt_i32 s12, 0
	s_cselect_b32 s14, s31, 0x160
	s_mul_i32 s12, s12, s14
	v_mfma_f32_16x16x32_bf16 v[78:81], v[146:149], v[220:223], 0
	s_add_i32 s12, s12, s13
	s_mul_hi_i32 s13, s12, 0x2e8ba2e9
	s_lshr_b32 s14, s13, 31
	v_mfma_f32_16x16x32_bf16 v[74:77], v[160:163], v[220:223], 0
	s_ashr_i32 s13, s13, 6
	s_add_i32 s13, s13, s14
	s_lshl_b32 s14, s13, 3
	v_mfma_f32_16x16x32_bf16 v[126:129], v[156:159], v[194:197], v[126:129]
	s_sub_i32 s15, 64, s14
	s_min_i32 s15, s15, 8
	s_abs_i32 s16, s15
	v_mfma_f32_16x16x32_bf16 v[122:125], v[164:167], v[194:197], v[122:125]
	v_cvt_f32_u32_e32 v250, s16
	s_sub_i32 s18, 0, s16
	s_mulk_i32 s13, 0x160
	v_mfma_f32_16x16x32_bf16 v[110:113], v[156:159], v[202:205], v[110:113]
	s_sub_i32 s13, s12, s13
	v_rcp_iflag_f32_e32 v250, v250
	s_abs_i32 s12, s13
	v_mfma_f32_16x16x32_bf16 v[106:109], v[164:167], v[202:205], v[106:109]
	s_xor_b32 s17, s13, s15
	s_ashr_i32 s17, s17, 31
	v_mul_f32_e32 v250, 0x4f7ffffe, v250
	v_mfma_f32_16x16x32_bf16 v[94:97], v[156:159], v[216:219], v[94:97]
	v_cvt_u32_f32_e32 v250, v250
	s_nop 0
	v_readfirstlane_b32 s19, v250
	v_mfma_f32_16x16x32_bf16 v[90:93], v[164:167], v[216:219], v[90:93]
	s_mul_i32 s18, s18, s19
	s_mul_hi_u32 s18, s19, s18
	s_add_i32 s19, s19, s18
	v_mfma_f32_16x16x32_bf16 v[78:81], v[156:159], v[224:227], v[78:81]
	s_mul_hi_u32 s18, s12, s19
	s_mul_i32 s19, s18, s16
	s_sub_i32 s12, s12, s19
	v_mfma_f32_16x16x32_bf16 v[74:77], v[164:167], v[224:227], v[74:77]
	s_add_i32 s98, s18, 1
	s_sub_i32 s19, s12, s16
	s_cmp_ge_u32 s12, s16
	s_setprio 0
	s_setprio 1
	v_mfma_f32_16x16x32_bf16 v[118:121], v[168:171], v[190:193], 0
	s_cselect_b32 s18, s98, s18
	s_cselect_b32 s12, s19, s12
	s_add_i32 s19, s18, 1
	v_mfma_f32_16x16x32_bf16 v[114:117], v[176:179], v[190:193], 0
	s_cmp_ge_u32 s12, s16
	s_cselect_b32 s12, s19, s18
	s_xor_b32 s12, s12, s17
	v_mfma_f32_16x16x32_bf16 v[102:105], v[168:171], v[198:201], 0
	s_sub_i32 s12, s12, s17
	s_mul_i32 s15, s12, s15
	s_sub_i32 s13, s13, s15
	v_mfma_f32_16x16x32_bf16 v[98:101], v[176:179], v[198:201], 0
	s_add_i32 s14, s14, s13
	s_ashr_i32 s15, s14, 31
	s_lshl_b64 s[16:17], s[14:15], 20
	v_mfma_f32_16x16x32_bf16 v[86:89], v[168:171], v[206:209], 0
	s_add_u32 s16, s70, s16
	s_addc_u32 s17, s71, s17
	s_and_b64 s[18:19], s[2:3], exec
	v_mfma_f32_16x16x32_bf16 v[82:85], v[176:179], v[206:209], 0
	s_cselect_b32 s15, s17, s23
	s_cselect_b32 s44, s16, s22
	s_ashr_i32 s13, s12, 31
	v_mfma_f32_16x16x32_bf16 v[70:73], v[168:171], v[220:223], 0
	s_lshl_b64 s[18:19], s[12:13], 20
	s_add_u32 s18, s11, s18
	s_addc_u32 s19, s28, s19
	v_mfma_f32_16x16x32_bf16 v[66:69], v[176:179], v[220:223], 0
	s_and_b64 s[98:99], s[2:3], exec
	s_cselect_b32 s13, s19, s25
	s_cselect_b32 s45, s18, s24
	v_mfma_f32_16x16x32_bf16 v[118:121], v[172:175], v[194:197], v[118:121]
	v_mfma_f32_16x16x32_bf16 v[114:117], v[180:183], v[194:197], v[114:117]
	v_mfma_f32_16x16x32_bf16 v[102:105], v[172:175], v[202:205], v[102:105]
	v_mfma_f32_16x16x32_bf16 v[98:101], v[180:183], v[202:205], v[98:101]
	v_mfma_f32_16x16x32_bf16 v[86:89], v[172:175], v[216:219], v[86:89]
	v_mfma_f32_16x16x32_bf16 v[82:85], v[180:183], v[216:219], v[82:85]
	v_mfma_f32_16x16x32_bf16 v[70:73], v[172:175], v[224:227], v[70:73]
	v_mfma_f32_16x16x32_bf16 v[66:69], v[180:183], v[224:227], v[66:69]
	s_setprio 0
	s_barrier
; #define PG8_STAGE(bufoff, gbase, voff) do { _Pragma("unroll") for (int _i = 0; _i < 2; ++_i) \
;         __builtin_amdgcn_global_load_lds((const unsigned*)((const char*)(gbase) + (voff)[_i]), (PG8_LAS unsigned*)(lds + (bufoff) + ldsw + _i * 8192), 16, 0, 0); } while (0)
; #define PG8_LDA(dst, b, h) do { _Pragma("unroll") for (int m = 0; m < 4; ++m) _Pragma("unroll") for (int k = 0; k < 2; ++k) dst[m][k] = *(const PG8_LAS bf16x8*)(lds + PG8_SA(b, h) + aoff + m * 2048 + k * 1024); } while (0)
; #define PG8_LDB(dst, b, h) do { _Pragma("unroll") for (int n = 0; n < 2; ++n) _Pragma("unroll") for (int k = 0; k < 2; ++k) dst[n][k] = *(const PG8_LAS bf16x8*)(lds + PG8_SB(b, h) + boff + n * 2048 + k * 1024); } while (0)
; #define PG8_WAIT_V(n) asm volatile("s_waitcnt vmcnt(" #n ")" ::: "memory")
; #define PG8_WAIT_L(n) asm volatile("s_waitcnt lgkmcnt(" #n ")" ::: "memory")
; #define PG8_BAR __builtin_amdgcn_s_barrier()
; #define PG8_SCHED __builtin_amdgcn_sched_barrier(0)
; template <class Epi, class Sched, bool ALIGN_EPI = false, bool SP2 = false>
; __device__ __forceinline__ void gemm_phase(PG8_LAS unsigned char* lds, const Gemm g, const Sched& S, const Epi& E) {
;     ...
;             PG8_LDA(At, 0, 1); PG8_STAGE(PG8_SB(0, 0), b2, voffB); PG8_STAGE(PG8_SB(0, 1), b2 + hstep, voffB); PG8_STAGE(PG8_SA(0, 0), a2, voffA);
;             PG8_WAIT_V(8); PG8_WAIT_L(0); PG8_BAR; PG8_MMA(1, 0, At, B0); PG8_MMA(1, 1, At, B1); PG8_BAR; PG8_SCHED;
;             PG8_LDB(B0, 1, 0); PG8_LDB(B1, 1, 1); PG8_SCHED; PG8_LDA(At, 1, 0); PG8_STAGE(PG8_SA(0, 1), a2 + hstep, voffA);
;             PG8_WAIT_V(8); PG8_WAIT_L(0); PG8_BAR; PG8_MMA(0, 0, At, B0); PG8_MMA(0, 1, At, B1); PG8_BAR; PG8_SCHED;
	s_add_i32 s49, s40, s29
	s_mov_b32 m0, s49
	ds_read_b128 v[190:193], v155 offset:16384
	ds_read_b128 v[194:197], v155 offset:17408
	ds_read_b128 v[198:201], v155 offset:18432
	ds_read_b128 v[202:205], v155 offset:19456
	ds_read_b128 v[206:209], v155 offset:20480
	ds_read_b128 v[216:219], v155 offset:21504
	ds_read_b128 v[220:223], v155 offset:22528
	ds_read_b128 v[224:227], v155 offset:23552
	global_load_lds_dwordx4 v134, s[24:25]
	s_add_i32 m0, s49, 0x2000
	s_add_u32 s50, s24, 0x80000
	s_addc_u32 s51, s25, 0
	s_add_i32 s49, s41, s29
	global_load_lds_dwordx4 v130, s[24:25]
	s_mov_b32 m0, s49
	s_nop 0
	global_load_lds_dwordx4 v134, s[50:51]
	s_add_i32 m0, s49, 0x2000
	s_nop 0
	global_load_lds_dwordx4 v130, s[50:51]
	s_mov_b32 m0, s21
	s_nop 0
	global_load_lds_dwordx4 v136, s[26:27]
	s_mov_b32 m0, s33
	s_nop 0
	global_load_lds_dwordx4 v132, s[26:27]
	s_waitcnt vmcnt(8)
	s_waitcnt lgkmcnt(0)
	s_barrier
	s_setprio 1
	s_waitcnt lgkmcnt(0)
	v_mfma_f32_16x16x32_bf16 v[62:65], v[146:149], v[190:193], 0
	v_mfma_f32_16x16x32_bf16 v[58:61], v[160:163], v[190:193], 0
	v_mfma_f32_16x16x32_bf16 v[46:49], v[146:149], v[198:201], 0
	v_mfma_f32_16x16x32_bf16 v[42:45], v[160:163], v[198:201], 0
	v_mfma_f32_16x16x32_bf16 v[30:33], v[146:149], v[206:209], 0
	v_mfma_f32_16x16x32_bf16 v[26:29], v[160:163], v[206:209], 0
	v_mfma_f32_16x16x32_bf16 v[14:17], v[146:149], v[220:223], 0
	v_mfma_f32_16x16x32_bf16 v[10:13], v[160:163], v[220:223], 0
	v_mfma_f32_16x16x32_bf16 v[62:65], v[156:159], v[194:197], v[62:65]
	v_mfma_f32_16x16x32_bf16 v[58:61], v[164:167], v[194:197], v[58:61]
	v_mfma_f32_16x16x32_bf16 v[46:49], v[156:159], v[202:205], v[46:49]
	v_mfma_f32_16x16x32_bf16 v[42:45], v[164:167], v[202:205], v[42:45]
	v_mfma_f32_16x16x32_bf16 v[30:33], v[156:159], v[216:219], v[30:33]
	v_mfma_f32_16x16x32_bf16 v[26:29], v[164:167], v[216:219], v[26:29]
	v_mfma_f32_16x16x32_bf16 v[14:17], v[156:159], v[224:227], v[14:17]
	v_mfma_f32_16x16x32_bf16 v[10:13], v[164:167], v[224:227], v[10:13]
	s_setprio 0
	s_setprio 1
	v_mfma_f32_16x16x32_bf16 v[54:57], v[168:171], v[190:193], 0
	v_mfma_f32_16x16x32_bf16 v[50:53], v[176:179], v[190:193], 0
	v_mfma_f32_16x16x32_bf16 v[38:41], v[168:171], v[198:201], 0
	v_mfma_f32_16x16x32_bf16 v[34:37], v[176:179], v[198:201], 0
	v_mfma_f32_16x16x32_bf16 v[22:25], v[168:171], v[206:209], 0
	v_mfma_f32_16x16x32_bf16 v[18:21], v[176:179], v[206:209], 0
	v_mfma_f32_16x16x32_bf16 v[6:9], v[168:171], v[220:223], 0
	v_mfma_f32_16x16x32_bf16 v[2:5], v[176:179], v[220:223], 0
	v_mfma_f32_16x16x32_bf16 v[54:57], v[172:175], v[194:197], v[54:57]
	v_mfma_f32_16x16x32_bf16 v[50:53], v[180:183], v[194:197], v[50:53]
	v_mfma_f32_16x16x32_bf16 v[38:41], v[172:175], v[202:205], v[38:41]
	v_mfma_f32_16x16x32_bf16 v[34:37], v[180:183], v[202:205], v[34:37]
	v_mfma_f32_16x16x32_bf16 v[22:25], v[172:175], v[216:219], v[22:25]
	v_mfma_f32_16x16x32_bf16 v[18:21], v[180:183], v[216:219], v[18:21]
	v_mfma_f32_16x16x32_bf16 v[6:9], v[172:175], v[224:227], v[6:9]
	v_mfma_f32_16x16x32_bf16 v[2:5], v[180:183], v[224:227], v[2:5]
	s_setprio 0
	s_barrier
	s_add_i32 s49, 0, 0x18000
	s_add_i32 s50, 0, 0x1c000
	ds_read_b128 v[146:149], v248
	ds_read_b128 v[156:159], v248 offset:1024
	ds_read_b128 v[160:163], v248 offset:2048
	ds_read_b128 v[164:167], v248 offset:3072
	ds_read_b128 v[168:171], v249
	ds_read_b128 v[172:175], v249 offset:1024
	ds_read_b128 v[176:179], v249 offset:2048
	ds_read_b128 v[180:183], v249 offset:3072
	s_add_u32 s26, s26, 0x80000
	s_addc_u32 s27, s27, 0
	s_mov_b32 m0, s34
	ds_read_b128 v[190:193], v155 offset:32768
	ds_read_b128 v[194:197], v155 offset:33792
	ds_read_b128 v[198:201], v155 offset:34816
	ds_read_b128 v[202:205], v155 offset:35840
	ds_read_b128 v[206:209], v155 offset:36864
	ds_read_b128 v[216:219], v155 offset:37888
	ds_read_b128 v[220:223], v155 offset:38912
	ds_read_b128 v[224:227], v155 offset:39936
	global_load_lds_dwordx4 v136, s[26:27]
	s_mov_b32 m0, s35
	s_nop 0
	global_load_lds_dwordx4 v132, s[26:27]
	s_waitcnt vmcnt(8)
	s_waitcnt lgkmcnt(0)
	s_barrier
; #define PG8_STAGE(bufoff, gbase, voff) do { _Pragma("unroll") for (int _i = 0; _i < 2; ++_i) \
;         __builtin_amdgcn_global_load_lds((const unsigned*)((const char*)(gbase) + (voff)[_i]), (PG8_LAS unsigned*)(lds + (bufoff) + ldsw + _i * 8192), 16, 0, 0); } while (0)
; #define PG8_LDA(dst, b, h) do { _Pragma("unroll") for (int m = 0; m < 4; ++m) _Pragma("unroll") for (int k = 0; k < 2; ++k) dst[m][k] = *(const PG8_LAS bf16x8*)(lds + PG8_SA(b, h) + aoff + m * 2048 + k * 1024); } while (0)
; #define PG8_WAIT_V(n) asm volatile("s_waitcnt vmcnt(" #n ")" ::: "memory")
; #define PG8_WAIT_L(n) asm volatile("s_waitcnt lgkmcnt(" #n ")" ::: "memory")
; #define PG8_BAR __builtin_amdgcn_s_barrier()
; #define PG8_SCHED __builtin_amdgcn_sched_barrier(0)
; template <class Epi, class Sched, bool ALIGN_EPI = false, bool SP2 = false>
; __device__ __forceinline__ void gemm_phase(PG8_LAS unsigned char* lds, const Gemm g, const Sched& S, const Epi& E) {
;     ...
;             PG8_WAIT_V(8); PG8_WAIT_L(0); PG8_BAR; PG8_MMA(0, 0, At, B0); PG8_MMA(0, 1, At, B1); PG8_BAR; PG8_SCHED;
;             PG8_LDA(At, 1, 1); PG8_STAGE(PG8_SB(1, 0), b3, voffB); PG8_STAGE(PG8_SB(1, 1), b3 + hstep, voffB); PG8_STAGE(PG8_SA(1, 0), a3, voffA);
;             PG8_WAIT_V(8); PG8_WAIT_L(0); PG8_BAR; PG8_MMA(1, 0, At, B0); PG8_MMA(1, 1, At, B1); PG8_BAR; PG8_SCHED;
	s_setprio 1
	s_waitcnt lgkmcnt(0)
	v_mfma_f32_16x16x32_bf16 v[126:129], v[146:149], v[190:193], v[126:129]
	v_mfma_f32_16x16x32_bf16 v[122:125], v[160:163], v[190:193], v[122:125]
	v_mfma_f32_16x16x32_bf16 v[110:113], v[146:149], v[198:201], v[110:113]
	v_mfma_f32_16x16x32_bf16 v[106:109], v[160:163], v[198:201], v[106:109]
	v_mfma_f32_16x16x32_bf16 v[94:97], v[146:149], v[206:209], v[94:97]
	v_mfma_f32_16x16x32_bf16 v[90:93], v[160:163], v[206:209], v[90:93]
	v_mfma_f32_16x16x32_bf16 v[78:81], v[146:149], v[220:223], v[78:81]
	v_mfma_f32_16x16x32_bf16 v[74:77], v[160:163], v[220:223], v[74:77]
	v_mfma_f32_16x16x32_bf16 v[126:129], v[156:159], v[194:197], v[126:129]
	v_mfma_f32_16x16x32_bf16 v[122:125], v[164:167], v[194:197], v[122:125]
	v_mfma_f32_16x16x32_bf16 v[110:113], v[156:159], v[202:205], v[110:113]
	v_mfma_f32_16x16x32_bf16 v[106:109], v[164:167], v[202:205], v[106:109]
	v_mfma_f32_16x16x32_bf16 v[94:97], v[156:159], v[216:219], v[94:97]
	v_mfma_f32_16x16x32_bf16 v[90:93], v[164:167], v[216:219], v[90:93]
	v_mfma_f32_16x16x32_bf16 v[78:81], v[156:159], v[224:227], v[78:81]
	v_mfma_f32_16x16x32_bf16 v[74:77], v[164:167], v[224:227], v[74:77]
	s_setprio 0
	s_setprio 1
	v_mfma_f32_16x16x32_bf16 v[118:121], v[168:171], v[190:193], v[118:121]
	v_mfma_f32_16x16x32_bf16 v[114:117], v[176:179], v[190:193], v[114:117]
	v_mfma_f32_16x16x32_bf16 v[102:105], v[168:171], v[198:201], v[102:105]
	v_mfma_f32_16x16x32_bf16 v[98:101], v[176:179], v[198:201], v[98:101]
	v_mfma_f32_16x16x32_bf16 v[86:89], v[168:171], v[206:209], v[86:89]
	v_mfma_f32_16x16x32_bf16 v[82:85], v[176:179], v[206:209], v[82:85]
	v_mfma_f32_16x16x32_bf16 v[70:73], v[168:171], v[220:223], v[70:73]
	v_mfma_f32_16x16x32_bf16 v[66:69], v[176:179], v[220:223], v[66:69]
	v_mfma_f32_16x16x32_bf16 v[118:121], v[172:175], v[194:197], v[118:121]
	v_mfma_f32_16x16x32_bf16 v[114:117], v[180:183], v[194:197], v[114:117]
	v_mfma_f32_16x16x32_bf16 v[102:105], v[172:175], v[202:205], v[102:105]
	v_mfma_f32_16x16x32_bf16 v[98:101], v[180:183], v[202:205], v[98:101]
	v_mfma_f32_16x16x32_bf16 v[86:89], v[172:175], v[216:219], v[86:89]
	v_mfma_f32_16x16x32_bf16 v[82:85], v[180:183], v[216:219], v[82:85]
	v_mfma_f32_16x16x32_bf16 v[70:73], v[172:175], v[224:227], v[70:73]
	v_mfma_f32_16x16x32_bf16 v[66:69], v[180:183], v[224:227], v[66:69]
	s_setprio 0
	s_barrier
	s_add_u32 s98, s24, 0x80
	s_addc_u32 s99, s25, 0
	s_add_u32 s100, s26, 0xfff80080
	s_addc_u32 s101, s27, -1
	s_add_i32 s26, s49, s29
	s_mov_b32 m0, s26
	ds_read_b128 v[190:193], v155 offset:49152
	ds_read_b128 v[194:197], v155 offset:50176
	ds_read_b128 v[198:201], v155 offset:51200
	ds_read_b128 v[202:205], v155 offset:52224
	ds_read_b128 v[206:209], v155 offset:53248
	ds_read_b128 v[216:219], v155 offset:54272
	ds_read_b128 v[220:223], v155 offset:55296
	ds_read_b128 v[224:227], v155 offset:56320
	global_load_lds_dwordx4 v134, s[98:99]
	s_add_i32 m0, s26, 0x2000
	s_add_u32 s24, s24, 0x80080
	s_addc_u32 s25, s25, 0
	s_add_i32 s26, s50, s29
	global_load_lds_dwordx4 v130, s[98:99]
	s_mov_b32 m0, s26
	s_nop 0
	global_load_lds_dwordx4 v134, s[24:25]
	s_add_i32 m0, s26, 0x2000
	s_nop 0
	global_load_lds_dwordx4 v130, s[24:25]
	s_mov_b32 m0, s37
	s_nop 0
	global_load_lds_dwordx4 v136, s[100:101]
	s_mov_b32 m0, s38
	s_nop 0
	global_load_lds_dwordx4 v132, s[100:101]
	s_waitcnt vmcnt(8)
	s_waitcnt lgkmcnt(0)
	s_barrier
	s_setprio 1
	s_waitcnt lgkmcnt(0)
	v_mfma_f32_16x16x32_bf16 v[62:65], v[146:149], v[190:193], v[62:65]
	v_mfma_f32_16x16x32_bf16 v[58:61], v[160:163], v[190:193], v[58:61]
	v_mfma_f32_16x16x32_bf16 v[46:49], v[146:149], v[198:201], v[46:49]
	v_mfma_f32_16x16x32_bf16 v[42:45], v[160:163], v[198:201], v[42:45]
	v_mfma_f32_16x16x32_bf16 v[30:33], v[146:149], v[206:209], v[30:33]
	v_mfma_f32_16x16x32_bf16 v[26:29], v[160:163], v[206:209], v[26:29]
	v_mfma_f32_16x16x32_bf16 v[14:17], v[146:149], v[220:223], v[14:17]
	v_mfma_f32_16x16x32_bf16 v[10:13], v[160:163], v[220:223], v[10:13]
	v_mfma_f32_16x16x32_bf16 v[62:65], v[156:159], v[194:197], v[62:65]
	v_mfma_f32_16x16x32_bf16 v[58:61], v[164:167], v[194:197], v[58:61]
	v_mfma_f32_16x16x32_bf16 v[46:49], v[156:159], v[202:205], v[46:49]
	v_mfma_f32_16x16x32_bf16 v[42:45], v[164:167], v[202:205], v[42:45]
	v_mfma_f32_16x16x32_bf16 v[30:33], v[156:159], v[216:219], v[30:33]
	v_mfma_f32_16x16x32_bf16 v[26:29], v[164:167], v[216:219], v[26:29]
	v_mfma_f32_16x16x32_bf16 v[14:17], v[156:159], v[224:227], v[14:17]
	v_mfma_f32_16x16x32_bf16 v[10:13], v[164:167], v[224:227], v[10:13]
	s_setprio 0
	s_setprio 1
	v_mfma_f32_16x16x32_bf16 v[54:57], v[168:171], v[190:193], v[54:57]
	v_mfma_f32_16x16x32_bf16 v[50:53], v[176:179], v[190:193], v[50:53]
	v_mfma_f32_16x16x32_bf16 v[38:41], v[168:171], v[198:201], v[38:41]
	v_mfma_f32_16x16x32_bf16 v[34:37], v[176:179], v[198:201], v[34:37]
	v_mfma_f32_16x16x32_bf16 v[22:25], v[168:171], v[206:209], v[22:25]
	v_mfma_f32_16x16x32_bf16 v[18:21], v[176:179], v[206:209], v[18:21]
	v_mfma_f32_16x16x32_bf16 v[6:9], v[168:171], v[220:223], v[6:9]
	v_mfma_f32_16x16x32_bf16 v[2:5], v[176:179], v[220:223], v[2:5]
	v_mfma_f32_16x16x32_bf16 v[54:57], v[172:175], v[194:197], v[54:57]
	v_mfma_f32_16x16x32_bf16 v[50:53], v[180:183], v[194:197], v[50:53]
	v_mfma_f32_16x16x32_bf16 v[38:41], v[172:175], v[202:205], v[38:41]
	v_mfma_f32_16x16x32_bf16 v[34:37], v[180:183], v[202:205], v[34:37]
	v_mfma_f32_16x16x32_bf16 v[22:25], v[172:175], v[216:219], v[22:25]
	v_mfma_f32_16x16x32_bf16 v[18:21], v[180:183], v[216:219], v[18:21]
	v_mfma_f32_16x16x32_bf16 v[6:9], v[172:175], v[224:227], v[6:9]
	v_mfma_f32_16x16x32_bf16 v[2:5], v[180:183], v[224:227], v[2:5]
	s_setprio 0
	s_barrier
	s_add_i32 s48, s48, 2
	s_add_u32 s22, s22, 0x100
	s_addc_u32 s23, s23, 0
	s_add_u32 s46, s46, 0x100
	s_addc_u32 s47, s47, 0
	s_cmp_gt_u32 s48, 29

; #define PG8_STAGE(bufoff, gbase, voff) do { _Pragma("unroll") for (int _i = 0; _i < 2; ++_i) \
;         __builtin_amdgcn_global_load_lds((const unsigned*)((const char*)(gbase) + (voff)[_i]), (PG8_LAS unsigned*)(lds + (bufoff) + ldsw + _i * 8192), 16, 0, 0); } while (0)
; #define PG8_LDA(dst, b, h) do { _Pragma("unroll") for (int m = 0; m < 4; ++m) _Pragma("unroll") for (int k = 0; k < 2; ++k) dst[m][k] = *(const PG8_LAS bf16x8*)(lds + PG8_SA(b, h) + aoff + m * 2048 + k * 1024); } while (0)
; #define PG8_LDB(dst, b, h) do { _Pragma("unroll") for (int n = 0; n < 2; ++n) _Pragma("unroll") for (int k = 0; k < 2; ++k) dst[n][k] = *(const PG8_LAS bf16x8*)(lds + PG8_SB(b, h) + boff + n * 2048 + k * 1024); } while (0)
; #define PG8_BAR __builtin_amdgcn_s_barrier()
;     __host__ __device__ bool next(int i, Unit& u) const {
;         const long L = (long)i * G + c; if (L >= nwg) return false;
;         int wgid = (int)L; { const int q = nwg / NXCD, r = nwg % NXCD, xcd = wgid % NXCD, off = wgid / NXCD; wgid = (xcd < r ? xcd * (q + 1) : r * (q + 1) + (xcd - r) * q) + off; }
;         const int nig = WGM * nN, gid = wgid / nig, fm = gid * WGM, gsz = (nM - fm) < WGM ? (nM - fm) : WGM;
;         u.pm = fm + ((wgid % nig) % gsz); u.pn = (wgid % nig) / gsz; return true;
;     }
; template <class Epi, class Sched, bool ALIGN_EPI = false, bool SP2 = false>
; __device__ __forceinline__ void gemm_phase(PG8_LAS unsigned char* lds, const Gemm g, const Sched& S, const Epi& E) {
;     ...
;         const bool has_next = S.next(ui + 1, nxt);
;         const char* nA = has_next ? (const char*)g.A + (size_t)nxt.pm * tstep : cA; const char* nB = has_next ? (const char*)g.Bt + (size_t)nxt.pn * tstep : cB;
;         for (int t = 0; t < nt; t += 2) {
;             const bool last = (t == nt - 2);
;             const char* a1 = cA + (size_t)(t + 1) * kstep;
;             const char* a2 = last ? nA : cA + (size_t)(t + 2) * kstep; const char* b2 = last ? nB : cB + (size_t)(t + 2) * kstep;
;             const char* a3 = a2 + kstep; const char* b3 = b2 + kstep;
;             if (last && has_next) S.a_ready(nxt);
;             if constexpr (SP2) {
;             PG8_LDB(B0, 0, 0); PG8_LDB(B1, 0, 1); PG8_SCHED; PG8_LDA(At, 0, 0); PG8_STAGE(PG8_SA(1, 1), a1 + hstep, voffA);
;             PG8_WAIT_V(8); PG8_WAIT_L(0); PG8_BAR; PG8_MMA(0, 0, At, B0); PG8_MMA(0, 1, At, B1); PG8_BAR; PG8_SCHED;
.LBB0_1073:
	s_add_u32 s30, s30, 0x80080
	s_addc_u32 s31, s31, 0
	s_add_u32 s56, s34, 0x100
	s_addc_u32 s57, s35, 0
	s_mov_b32 s58, -2
	v_add_u32_e32 v248, 0x18000, v155
	v_add_u32_e32 v249, 0x1c000, v155
	ds_read_b128 v[148:151], v157
	ds_read_b128 v[160:163], v157 offset:1024
	ds_read_b128 v[164:167], v157 offset:2048
	ds_read_b128 v[168:171], v157 offset:3072
	ds_read_b128 v[172:175], v158
	ds_read_b128 v[176:179], v158 offset:1024
	ds_read_b128 v[180:183], v158 offset:2048
	ds_read_b128 v[190:193], v158 offset:3072
	s_add_u32 s34, s30, 0xfff80080
	s_addc_u32 s35, s31, -1
	s_cmp_eq_u32 s58, 28
	s_cselect_b32 s37, s23, s35
	s_cselect_b32 s36, s29, s34
	s_cselect_b32 s35, s21, s57
	s_cselect_b32 s34, s55, s56
	s_add_i32 m0, s42, 0xc000
	ds_read_b128 v[194:197], v159
	ds_read_b128 v[198:201], v159 offset:1024
	ds_read_b128 v[202:205], v159 offset:2048
	ds_read_b128 v[206:209], v159 offset:3072
	ds_read_b128 v[216:219], v159 offset:4096
	ds_read_b128 v[220:223], v159 offset:5120
	ds_read_b128 v[224:227], v159 offset:6144
	ds_read_b128 v[228:231], v159 offset:7168
	global_load_lds_dwordx4 v140, s[30:31]
	s_add_i32 m0, s42, 0xe000
	s_nop 0
	global_load_lds_dwordx4 v142, s[30:31]
	s_waitcnt vmcnt(8)
	s_waitcnt lgkmcnt(0)
	s_barrier
	s_setprio 1
	s_waitcnt lgkmcnt(0)
	v_mfma_f32_16x16x32_bf16 v[126:129], v[148:151], v[194:197], 0
	s_add_i32 s46, s46, 1
	s_mul_i32 s2, s46, s50
	s_mul_hi_u32 s3, s46, s82
	v_mfma_f32_16x16x32_bf16 v[122:125], v[164:167], v[194:197], 0
	s_add_i32 s3, s3, s2
	s_mul_i32 s2, s46, s82
	v_readlane_b32 s21, v247, 6
	v_mfma_f32_16x16x32_bf16 v[118:121], v[148:151], v[202:205], 0
	s_add_u32 s24, s2, s21
	s_addc_u32 s25, s3, s40
	v_cmp_lt_i64_e64 s[2:3], s[24:25], v[144:145]
	v_mfma_f32_16x16x32_bf16 v[110:113], v[164:167], v[202:205], 0
	s_ashr_i32 s20, s24, 31
	s_lshr_b32 s20, s20, 29
	s_add_i32 s20, s24, s20
	v_mfma_f32_16x16x32_bf16 v[102:105], v[148:151], v[216:219], 0
	s_ashr_i32 s21, s20, 3
	s_and_b32 s20, s20, -8
	s_sub_i32 s20, s24, s20
	v_mfma_f32_16x16x32_bf16 v[94:97], v[164:167], v[216:219], 0
	s_cmp_lt_i32 s20, 0
	s_cselect_b32 s22, s41, 0x90
	s_mul_i32 s20, s20, s22
	v_mfma_f32_16x16x32_bf16 v[86:89], v[148:151], v[224:227], 0
	s_add_i32 s20, s20, s21
	s_mul_hi_i32 s21, s20, 0x38e38e39
	s_lshr_b32 s22, s21, 31
	v_mfma_f32_16x16x32_bf16 v[78:81], v[164:167], v[224:227], 0
	s_ashr_i32 s21, s21, 5
	s_add_i32 s21, s21, s22
	s_lshl_b32 s22, s21, 3
	v_mfma_f32_16x16x32_bf16 v[126:129], v[160:163], v[198:201], v[126:129]
	s_sub_i32 s23, 64, s22
	s_min_i32 s23, s23, 8
	s_abs_i32 s24, s23
	v_mfma_f32_16x16x32_bf16 v[122:125], v[168:171], v[198:201], v[122:125]
	v_cvt_f32_u32_e32 v250, s24
	s_sub_i32 s26, 0, s24
	s_mulk_i32 s21, 0x90
	v_mfma_f32_16x16x32_bf16 v[118:121], v[160:163], v[206:209], v[118:121]
	s_sub_i32 s21, s20, s21
	v_rcp_iflag_f32_e32 v250, v250
	s_abs_i32 s20, s21
	v_mfma_f32_16x16x32_bf16 v[110:113], v[168:171], v[206:209], v[110:113]
	s_xor_b32 s25, s21, s23
	s_ashr_i32 s25, s25, 31
	v_mul_f32_e32 v250, 0x4f7ffffe, v250
	v_mfma_f32_16x16x32_bf16 v[102:105], v[160:163], v[220:223], v[102:105]
	v_cvt_u32_f32_e32 v250, v250
	s_nop 0
	v_readfirstlane_b32 s27, v250
	v_mfma_f32_16x16x32_bf16 v[94:97], v[168:171], v[220:223], v[94:97]
	s_mul_i32 s26, s26, s27
	s_mul_hi_u32 s26, s27, s26
	s_add_i32 s27, s27, s26
	v_mfma_f32_16x16x32_bf16 v[86:89], v[160:163], v[228:231], v[86:89]
	s_mul_hi_u32 s26, s20, s27
	s_mul_i32 s27, s26, s24
	s_sub_i32 s20, s20, s27
	v_mfma_f32_16x16x32_bf16 v[78:81], v[168:171], v[228:231], v[78:81]
	s_add_i32 s29, s26, 1
	s_sub_i32 s27, s20, s24
	s_cmp_ge_u32 s20, s24
	s_setprio 0
	s_setprio 1
	v_mfma_f32_16x16x32_bf16 v[114:117], v[172:175], v[194:197], 0
	s_cselect_b32 s26, s29, s26
	s_cselect_b32 s20, s27, s20
	s_add_i32 s27, s26, 1
	v_mfma_f32_16x16x32_bf16 v[106:109], v[180:183], v[194:197], 0
	s_cmp_ge_u32 s20, s24
	s_cselect_b32 s20, s27, s26
	s_xor_b32 s20, s20, s25
	v_mfma_f32_16x16x32_bf16 v[98:101], v[172:175], v[202:205], 0
	s_sub_i32 s20, s20, s25
	s_mul_i32 s23, s20, s23
	s_sub_i32 s21, s21, s23
	v_mfma_f32_16x16x32_bf16 v[90:93], v[180:183], v[202:205], 0
	s_add_i32 s22, s22, s21
	s_ashr_i32 s23, s22, 31
	s_lshl_b64 s[24:25], s[22:23], 20
	v_mfma_f32_16x16x32_bf16 v[82:85], v[172:175], v[216:219], 0
	s_add_u32 s24, s70, s24
	s_addc_u32 s25, s71, s25
	s_and_b64 s[26:27], s[2:3], exec
	v_mfma_f32_16x16x32_bf16 v[74:77], v[180:183], v[216:219], 0
	s_cselect_b32 s23, s25, s31
	s_cselect_b32 s29, s24, s30
	s_ashr_i32 s21, s20, 31
	v_mfma_f32_16x16x32_bf16 v[70:73], v[172:175], v[224:227], 0
	s_lshl_b64 s[26:27], s[20:21], 20
	s_add_u32 s26, s33, s26
	s_addc_u32 s27, s38, s27
	v_mfma_f32_16x16x32_bf16 v[66:69], v[180:183], v[224:227], 0
	s_and_b64 s[98:99], s[2:3], exec
	s_cselect_b32 s21, s27, s35
	s_cselect_b32 s55, s26, s34
	v_mfma_f32_16x16x32_bf16 v[114:117], v[176:179], v[198:201], v[114:117]
	v_mfma_f32_16x16x32_bf16 v[106:109], v[190:193], v[198:201], v[106:109]
	v_mfma_f32_16x16x32_bf16 v[98:101], v[176:179], v[206:209], v[98:101]
	v_mfma_f32_16x16x32_bf16 v[90:93], v[190:193], v[206:209], v[90:93]
	v_mfma_f32_16x16x32_bf16 v[82:85], v[176:179], v[220:223], v[82:85]
	v_mfma_f32_16x16x32_bf16 v[74:77], v[190:193], v[220:223], v[74:77]
	v_mfma_f32_16x16x32_bf16 v[70:73], v[176:179], v[228:231], v[70:73]
	v_mfma_f32_16x16x32_bf16 v[66:69], v[190:193], v[228:231], v[66:69]
	s_setprio 0
	s_barrier
; #define PG8_STAGE(bufoff, gbase, voff) do { _Pragma("unroll") for (int _i = 0; _i < 2; ++_i) \
;         __builtin_amdgcn_global_load_lds((const unsigned*)((const char*)(gbase) + (voff)[_i]), (PG8_LAS unsigned*)(lds + (bufoff) + ldsw + _i * 8192), 16, 0, 0); } while (0)
; #define PG8_LDA(dst, b, h) do { _Pragma("unroll") for (int m = 0; m < 4; ++m) _Pragma("unroll") for (int k = 0; k < 2; ++k) dst[m][k] = *(const PG8_LAS bf16x8*)(lds + PG8_SA(b, h) + aoff + m * 2048 + k * 1024); } while (0)
; #define PG8_LDB(dst, b, h) do { _Pragma("unroll") for (int n = 0; n < 2; ++n) _Pragma("unroll") for (int k = 0; k < 2; ++k) dst[n][k] = *(const PG8_LAS bf16x8*)(lds + PG8_SB(b, h) + boff + n * 2048 + k * 1024); } while (0)
; #define PG8_WAIT_V(n) asm volatile("s_waitcnt vmcnt(" #n ")" ::: "memory")
; #define PG8_WAIT_L(n) asm volatile("s_waitcnt lgkmcnt(" #n ")" ::: "memory")
; #define PG8_BAR __builtin_amdgcn_s_barrier()
; #define PG8_SCHED __builtin_amdgcn_sched_barrier(0)
; template <class Epi, class Sched, bool ALIGN_EPI = false, bool SP2 = false>
; __device__ __forceinline__ void gemm_phase(PG8_LAS unsigned char* lds, const Gemm g, const Sched& S, const Epi& E) {
;     ...
;             PG8_LDA(At, 0, 1); PG8_STAGE(PG8_SB(0, 0), b2, voffB); PG8_STAGE(PG8_SB(0, 1), b2 + hstep, voffB); PG8_STAGE(PG8_SA(0, 0), a2, voffA);
;             PG8_WAIT_V(8); PG8_WAIT_L(0); PG8_BAR; PG8_MMA(1, 0, At, B0); PG8_MMA(1, 1, At, B1); PG8_BAR; PG8_SCHED;
;             PG8_LDB(B0, 1, 0); PG8_LDB(B1, 1, 1); PG8_SCHED; PG8_LDA(At, 1, 0); PG8_STAGE(PG8_SA(0, 1), a2 + hstep, voffA);
;             PG8_WAIT_V(8); PG8_WAIT_L(0); PG8_BAR; PG8_MMA(0, 0, At, B0); PG8_MMA(0, 1, At, B1); PG8_BAR; PG8_SCHED;
	s_add_i32 s59, s51, s39
	s_mov_b32 m0, s59
	ds_read_b128 v[194:197], v159 offset:16384
	ds_read_b128 v[198:201], v159 offset:17408
	ds_read_b128 v[202:205], v159 offset:18432
	ds_read_b128 v[206:209], v159 offset:19456
	ds_read_b128 v[216:219], v159 offset:20480
	ds_read_b128 v[220:223], v159 offset:21504
	ds_read_b128 v[224:227], v159 offset:22528
	ds_read_b128 v[228:231], v159 offset:23552
	global_load_lds_dwordx4 v134, s[34:35]
	s_add_i32 m0, s59, 0x2000
	s_add_u32 s60, s34, 0x80000
	s_addc_u32 s61, s35, 0
	s_add_i32 s59, s52, s39
	global_load_lds_dwordx4 v130, s[34:35]
	s_mov_b32 m0, s59
	s_nop 0
	global_load_lds_dwordx4 v134, s[60:61]
	s_add_i32 m0, s59, 0x2000
	s_nop 0
	global_load_lds_dwordx4 v130, s[60:61]
	s_mov_b32 m0, s42
	s_nop 0
	global_load_lds_dwordx4 v136, s[36:37]
	s_mov_b32 m0, s43
	s_nop 0
	global_load_lds_dwordx4 v132, s[36:37]
	s_waitcnt vmcnt(8)
	s_waitcnt lgkmcnt(0)
	s_barrier
	s_setprio 1
	s_waitcnt lgkmcnt(0)
	v_mfma_f32_16x16x32_bf16 v[62:65], v[148:151], v[194:197], 0
	v_mfma_f32_16x16x32_bf16 v[58:61], v[164:167], v[194:197], 0
	v_mfma_f32_16x16x32_bf16 v[54:57], v[148:151], v[202:205], 0
	v_mfma_f32_16x16x32_bf16 v[46:49], v[164:167], v[202:205], 0
	v_mfma_f32_16x16x32_bf16 v[38:41], v[148:151], v[216:219], 0
	v_mfma_f32_16x16x32_bf16 v[30:33], v[164:167], v[216:219], 0
	v_mfma_f32_16x16x32_bf16 v[22:25], v[148:151], v[224:227], 0
	v_mfma_f32_16x16x32_bf16 v[14:17], v[164:167], v[224:227], 0
	v_mfma_f32_16x16x32_bf16 v[62:65], v[160:163], v[198:201], v[62:65]
	v_mfma_f32_16x16x32_bf16 v[58:61], v[168:171], v[198:201], v[58:61]
	v_mfma_f32_16x16x32_bf16 v[54:57], v[160:163], v[206:209], v[54:57]
	v_mfma_f32_16x16x32_bf16 v[46:49], v[168:171], v[206:209], v[46:49]
	v_mfma_f32_16x16x32_bf16 v[38:41], v[160:163], v[220:223], v[38:41]
	v_mfma_f32_16x16x32_bf16 v[30:33], v[168:171], v[220:223], v[30:33]
	v_mfma_f32_16x16x32_bf16 v[22:25], v[160:163], v[228:231], v[22:25]
	v_mfma_f32_16x16x32_bf16 v[14:17], v[168:171], v[228:231], v[14:17]
	s_setprio 0
	s_setprio 1
	v_mfma_f32_16x16x32_bf16 v[50:53], v[172:175], v[194:197], 0
	v_mfma_f32_16x16x32_bf16 v[42:45], v[180:183], v[194:197], 0
	v_mfma_f32_16x16x32_bf16 v[34:37], v[172:175], v[202:205], 0
	v_mfma_f32_16x16x32_bf16 v[26:29], v[180:183], v[202:205], 0
	v_mfma_f32_16x16x32_bf16 v[18:21], v[172:175], v[216:219], 0
	v_mfma_f32_16x16x32_bf16 v[10:13], v[180:183], v[216:219], 0
	v_mfma_f32_16x16x32_bf16 v[6:9], v[172:175], v[224:227], 0
	v_mfma_f32_16x16x32_bf16 v[2:5], v[180:183], v[224:227], 0
	v_mfma_f32_16x16x32_bf16 v[50:53], v[176:179], v[198:201], v[50:53]
	v_mfma_f32_16x16x32_bf16 v[42:45], v[190:193], v[198:201], v[42:45]
	v_mfma_f32_16x16x32_bf16 v[34:37], v[176:179], v[206:209], v[34:37]
	v_mfma_f32_16x16x32_bf16 v[26:29], v[190:193], v[206:209], v[26:29]
	v_mfma_f32_16x16x32_bf16 v[18:21], v[176:179], v[220:223], v[18:21]
	v_mfma_f32_16x16x32_bf16 v[10:13], v[190:193], v[220:223], v[10:13]
	v_mfma_f32_16x16x32_bf16 v[6:9], v[176:179], v[228:231], v[6:9]
	v_mfma_f32_16x16x32_bf16 v[2:5], v[190:193], v[228:231], v[2:5]
	s_setprio 0
	s_barrier
	s_add_i32 s59, 0, 0x18000
	s_add_i32 s60, 0, 0x1c000
	ds_read_b128 v[148:151], v248
	ds_read_b128 v[160:163], v248 offset:1024
	ds_read_b128 v[164:167], v248 offset:2048
	ds_read_b128 v[168:171], v248 offset:3072
	ds_read_b128 v[172:175], v249
	ds_read_b128 v[176:179], v249 offset:1024
	ds_read_b128 v[180:183], v249 offset:2048
	ds_read_b128 v[190:193], v249 offset:3072
	s_add_u32 s36, s36, 0x80000
	s_addc_u32 s37, s37, 0
	s_mov_b32 m0, s44
	ds_read_b128 v[194:197], v159 offset:32768
	ds_read_b128 v[198:201], v159 offset:33792
	ds_read_b128 v[202:205], v159 offset:34816
	ds_read_b128 v[206:209], v159 offset:35840
	ds_read_b128 v[216:219], v159 offset:36864
	ds_read_b128 v[220:223], v159 offset:37888
	ds_read_b128 v[224:227], v159 offset:38912
	ds_read_b128 v[228:231], v159 offset:39936
	global_load_lds_dwordx4 v136, s[36:37]
	s_mov_b32 m0, s45
	s_nop 0
	global_load_lds_dwordx4 v132, s[36:37]
	s_waitcnt vmcnt(8)
	s_waitcnt lgkmcnt(0)
	s_barrier
; #define PG8_STAGE(bufoff, gbase, voff) do { _Pragma("unroll") for (int _i = 0; _i < 2; ++_i) \
;         __builtin_amdgcn_global_load_lds((const unsigned*)((const char*)(gbase) + (voff)[_i]), (PG8_LAS unsigned*)(lds + (bufoff) + ldsw + _i * 8192), 16, 0, 0); } while (0)
; #define PG8_LDA(dst, b, h) do { _Pragma("unroll") for (int m = 0; m < 4; ++m) _Pragma("unroll") for (int k = 0; k < 2; ++k) dst[m][k] = *(const PG8_LAS bf16x8*)(lds + PG8_SA(b, h) + aoff + m * 2048 + k * 1024); } while (0)
; #define PG8_WAIT_V(n) asm volatile("s_waitcnt vmcnt(" #n ")" ::: "memory")
; #define PG8_WAIT_L(n) asm volatile("s_waitcnt lgkmcnt(" #n ")" ::: "memory")
; #define PG8_BAR __builtin_amdgcn_s_barrier()
; #define PG8_SCHED __builtin_amdgcn_sched_barrier(0)
; template <class Epi, class Sched, bool ALIGN_EPI = false, bool SP2 = false>
; __device__ __forceinline__ void gemm_phase(PG8_LAS unsigned char* lds, const Gemm g, const Sched& S, const Epi& E) {
;     ...
;             PG8_WAIT_V(8); PG8_WAIT_L(0); PG8_BAR; PG8_MMA(0, 0, At, B0); PG8_MMA(0, 1, At, B1); PG8_BAR; PG8_SCHED;
;             PG8_LDA(At, 1, 1); PG8_STAGE(PG8_SB(1, 0), b3, voffB); PG8_STAGE(PG8_SB(1, 1), b3 + hstep, voffB); PG8_STAGE(PG8_SA(1, 0), a3, voffA);
;             PG8_WAIT_V(8); PG8_WAIT_L(0); PG8_BAR; PG8_MMA(1, 0, At, B0); PG8_MMA(1, 1, At, B1); PG8_BAR; PG8_SCHED;
	s_setprio 1
	s_waitcnt lgkmcnt(0)
	v_mfma_f32_16x16x32_bf16 v[126:129], v[148:151], v[194:197], v[126:129]
	v_mfma_f32_16x16x32_bf16 v[122:125], v[164:167], v[194:197], v[122:125]
	v_mfma_f32_16x16x32_bf16 v[118:121], v[148:151], v[202:205], v[118:121]
	v_mfma_f32_16x16x32_bf16 v[110:113], v[164:167], v[202:205], v[110:113]
	v_mfma_f32_16x16x32_bf16 v[102:105], v[148:151], v[216:219], v[102:105]
	v_mfma_f32_16x16x32_bf16 v[94:97], v[164:167], v[216:219], v[94:97]
	v_mfma_f32_16x16x32_bf16 v[86:89], v[148:151], v[224:227], v[86:89]
	v_mfma_f32_16x16x32_bf16 v[78:81], v[164:167], v[224:227], v[78:81]
	v_mfma_f32_16x16x32_bf16 v[126:129], v[160:163], v[198:201], v[126:129]
	v_mfma_f32_16x16x32_bf16 v[122:125], v[168:171], v[198:201], v[122:125]
	v_mfma_f32_16x16x32_bf16 v[118:121], v[160:163], v[206:209], v[118:121]
	v_mfma_f32_16x16x32_bf16 v[110:113], v[168:171], v[206:209], v[110:113]
	v_mfma_f32_16x16x32_bf16 v[102:105], v[160:163], v[220:223], v[102:105]
	v_mfma_f32_16x16x32_bf16 v[94:97], v[168:171], v[220:223], v[94:97]
	v_mfma_f32_16x16x32_bf16 v[86:89], v[160:163], v[228:231], v[86:89]
	v_mfma_f32_16x16x32_bf16 v[78:81], v[168:171], v[228:231], v[78:81]
	s_setprio 0
	s_setprio 1
	v_mfma_f32_16x16x32_bf16 v[114:117], v[172:175], v[194:197], v[114:117]
	v_mfma_f32_16x16x32_bf16 v[106:109], v[180:183], v[194:197], v[106:109]
	v_mfma_f32_16x16x32_bf16 v[98:101], v[172:175], v[202:205], v[98:101]
	v_mfma_f32_16x16x32_bf16 v[90:93], v[180:183], v[202:205], v[90:93]
	v_mfma_f32_16x16x32_bf16 v[82:85], v[172:175], v[216:219], v[82:85]
	v_mfma_f32_16x16x32_bf16 v[74:77], v[180:183], v[216:219], v[74:77]
	v_mfma_f32_16x16x32_bf16 v[70:73], v[172:175], v[224:227], v[70:73]
	v_mfma_f32_16x16x32_bf16 v[66:69], v[180:183], v[224:227], v[66:69]
	v_mfma_f32_16x16x32_bf16 v[114:117], v[176:179], v[198:201], v[114:117]
	v_mfma_f32_16x16x32_bf16 v[106:109], v[190:193], v[198:201], v[106:109]
	v_mfma_f32_16x16x32_bf16 v[98:101], v[176:179], v[206:209], v[98:101]
	v_mfma_f32_16x16x32_bf16 v[90:93], v[190:193], v[206:209], v[90:93]
	v_mfma_f32_16x16x32_bf16 v[82:85], v[176:179], v[220:223], v[82:85]
	v_mfma_f32_16x16x32_bf16 v[74:77], v[190:193], v[220:223], v[74:77]
	v_mfma_f32_16x16x32_bf16 v[70:73], v[176:179], v[228:231], v[70:73]
	v_mfma_f32_16x16x32_bf16 v[66:69], v[190:193], v[228:231], v[66:69]
	s_setprio 0
	s_barrier
	s_add_u32 s98, s34, 0x80
	s_addc_u32 s99, s35, 0
	s_add_u32 s100, s36, 0xfff80080
	s_addc_u32 s101, s37, -1
	s_add_i32 s36, s59, s39
	s_mov_b32 m0, s36
	ds_read_b128 v[194:197], v159 offset:49152
	ds_read_b128 v[198:201], v159 offset:50176
	ds_read_b128 v[202:205], v159 offset:51200
	ds_read_b128 v[206:209], v159 offset:52224
	ds_read_b128 v[216:219], v159 offset:53248
	ds_read_b128 v[220:223], v159 offset:54272
	ds_read_b128 v[224:227], v159 offset:55296
	ds_read_b128 v[228:231], v159 offset:56320
	global_load_lds_dwordx4 v134, s[98:99]
	s_add_i32 m0, s36, 0x2000
	s_add_u32 s34, s34, 0x80080
	s_addc_u32 s35, s35, 0
	s_add_i32 s36, s60, s39
	global_load_lds_dwordx4 v130, s[98:99]
	s_mov_b32 m0, s36
	s_nop 0
	global_load_lds_dwordx4 v134, s[34:35]
	s_add_i32 m0, s36, 0x2000
	s_nop 0
	global_load_lds_dwordx4 v130, s[34:35]
	s_mov_b32 m0, s48
	s_nop 0
	global_load_lds_dwordx4 v136, s[100:101]
	s_mov_b32 m0, s49
	s_nop 0
	global_load_lds_dwordx4 v132, s[100:101]
	s_waitcnt vmcnt(8)
	s_waitcnt lgkmcnt(0)
	s_barrier
	s_setprio 1
	s_waitcnt lgkmcnt(0)
	v_mfma_f32_16x16x32_bf16 v[62:65], v[148:151], v[194:197], v[62:65]
	v_mfma_f32_16x16x32_bf16 v[58:61], v[164:167], v[194:197], v[58:61]
	v_mfma_f32_16x16x32_bf16 v[54:57], v[148:151], v[202:205], v[54:57]
	v_mfma_f32_16x16x32_bf16 v[46:49], v[164:167], v[202:205], v[46:49]
	v_mfma_f32_16x16x32_bf16 v[38:41], v[148:151], v[216:219], v[38:41]
	v_mfma_f32_16x16x32_bf16 v[30:33], v[164:167], v[216:219], v[30:33]
	v_mfma_f32_16x16x32_bf16 v[22:25], v[148:151], v[224:227], v[22:25]
	v_mfma_f32_16x16x32_bf16 v[14:17], v[164:167], v[224:227], v[14:17]
	v_mfma_f32_16x16x32_bf16 v[62:65], v[160:163], v[198:201], v[62:65]
	v_mfma_f32_16x16x32_bf16 v[58:61], v[168:171], v[198:201], v[58:61]
	v_mfma_f32_16x16x32_bf16 v[54:57], v[160:163], v[206:209], v[54:57]
	v_mfma_f32_16x16x32_bf16 v[46:49], v[168:171], v[206:209], v[46:49]
	v_mfma_f32_16x16x32_bf16 v[38:41], v[160:163], v[220:223], v[38:41]
	v_mfma_f32_16x16x32_bf16 v[30:33], v[168:171], v[220:223], v[30:33]
	v_mfma_f32_16x16x32_bf16 v[22:25], v[160:163], v[228:231], v[22:25]
	v_mfma_f32_16x16x32_bf16 v[14:17], v[168:171], v[228:231], v[14:17]
	s_setprio 0
	s_setprio 1
	v_mfma_f32_16x16x32_bf16 v[50:53], v[172:175], v[194:197], v[50:53]
	v_mfma_f32_16x16x32_bf16 v[42:45], v[180:183], v[194:197], v[42:45]
	v_mfma_f32_16x16x32_bf16 v[34:37], v[172:175], v[202:205], v[34:37]
	v_mfma_f32_16x16x32_bf16 v[26:29], v[180:183], v[202:205], v[26:29]
	v_mfma_f32_16x16x32_bf16 v[18:21], v[172:175], v[216:219], v[18:21]
	v_mfma_f32_16x16x32_bf16 v[10:13], v[180:183], v[216:219], v[10:13]
	v_mfma_f32_16x16x32_bf16 v[6:9], v[172:175], v[224:227], v[6:9]
	v_mfma_f32_16x16x32_bf16 v[2:5], v[180:183], v[224:227], v[2:5]
	v_mfma_f32_16x16x32_bf16 v[50:53], v[176:179], v[198:201], v[50:53]
	v_mfma_f32_16x16x32_bf16 v[42:45], v[190:193], v[198:201], v[42:45]
	v_mfma_f32_16x16x32_bf16 v[34:37], v[176:179], v[206:209], v[34:37]
	v_mfma_f32_16x16x32_bf16 v[26:29], v[190:193], v[206:209], v[26:29]
	v_mfma_f32_16x16x32_bf16 v[18:21], v[176:179], v[220:223], v[18:21]
	v_mfma_f32_16x16x32_bf16 v[10:13], v[190:193], v[220:223], v[10:13]
	v_mfma_f32_16x16x32_bf16 v[6:9], v[176:179], v[228:231], v[6:9]
	v_mfma_f32_16x16x32_bf16 v[2:5], v[190:193], v[228:231], v[2:5]
	s_setprio 0
	s_barrier
	s_add_i32 s58, s58, 2
	s_add_u32 s30, s30, 0x100
	s_addc_u32 s31, s31, 0
	s_add_u32 s56, s56, 0x100
	s_addc_u32 s57, s57, 0
	s_cmp_gt_u32 s58, 29

; #define PG8_STAGE(bufoff, gbase, voff) do { _Pragma("unroll") for (int _i = 0; _i < 2; ++_i) \
;         __builtin_amdgcn_global_load_lds((const unsigned*)((const char*)(gbase) + (voff)[_i]), (PG8_LAS unsigned*)(lds + (bufoff) + ldsw + _i * 8192), 16, 0, 0); } while (0)
; #define PG8_LDA(dst, b, h) do { _Pragma("unroll") for (int m = 0; m < 4; ++m) _Pragma("unroll") for (int k = 0; k < 2; ++k) dst[m][k] = *(const PG8_LAS bf16x8*)(lds + PG8_SA(b, h) + aoff + m * 2048 + k * 1024); } while (0)
; #define PG8_LDB(dst, b, h) do { _Pragma("unroll") for (int n = 0; n < 2; ++n) _Pragma("unroll") for (int k = 0; k < 2; ++k) dst[n][k] = *(const PG8_LAS bf16x8*)(lds + PG8_SB(b, h) + boff + n * 2048 + k * 1024); } while (0)
;     __device__ __forceinline__ bool next(int i, Unit& u) const {
;         const long L = (long)Lbase + (long)i * G + c; if (L >= Lend) return false;
;         int wgid = (int)L; { const int q = nwg / NXCD, r = nwg % NXCD, xcd = wgid % NXCD, off = wgid / NXCD; wgid = (xcd < r ? xcd * (q + 1) : r * (q + 1) + (xcd - r) * q) + off; }
;         const int nig = WGM * nN, gid = wgid / nig, fm = gid * WGM, gsz = (nM - fm) < WGM ? (nM - fm) : WGM;
;         u.pm = pm0 + fm + ((wgid % nig) % gsz); u.pn = tile_e[u.pm] * nN + (wgid % nig) / gsz; return true;
;     }
; template <class Epi, class Sched, bool ALIGN_EPI = false, bool SP2 = false>
; __device__ __forceinline__ void gemm_phase(PG8_LAS unsigned char* lds, const Gemm g, const Sched& S, const Epi& E) {
;     ...
;         const bool has_next = S.next(ui + 1, nxt);
;         const char* nA = has_next ? (const char*)g.A + (size_t)nxt.pm * tstep : cA; const char* nB = has_next ? (const char*)g.Bt + (size_t)nxt.pn * tstep : cB;
;         for (int t = 0; t < nt; t += 2) {
;             const bool last = (t == nt - 2);
;             const char* a1 = cA + (size_t)(t + 1) * kstep;
;             const char* a2 = last ? nA : cA + (size_t)(t + 2) * kstep; const char* b2 = last ? nB : cB + (size_t)(t + 2) * kstep;
;             const char* a3 = a2 + kstep; const char* b3 = b2 + kstep;
;             if (last && has_next) S.a_ready(nxt);
;             if constexpr (SP2) {
;             PG8_LDB(B0, 0, 0); PG8_LDB(B1, 0, 1); PG8_SCHED; PG8_LDA(At, 0, 0); PG8_STAGE(PG8_SA(1, 1), a1 + hstep, voffA);
;             PG8_WAIT_V(8); PG8_WAIT_L(0); PG8_BAR; PG8_MMA(0, 0, At, B0); PG8_MMA(0, 1, At, B1); PG8_BAR; PG8_SCHED;
.LBB0_1880:
	s_add_u32 s26, s26, 0x40080
	s_addc_u32 s27, s27, 0
	s_add_u32 s51, s28, 0x100
	s_addc_u32 s52, s29, 0
	s_mov_b32 s53, -2
	v_add_u32_e32 v248, 0x18000, v188
	v_add_u32_e32 v249, 0x1c000, v188
	ds_read_b128 v[26:29], v190
	ds_read_b128 v[30:33], v190 offset:1024
	ds_read_b128 v[18:21], v190 offset:2048
	ds_read_b128 v[22:25], v190 offset:3072
	ds_read_b128 v[10:13], v191
	ds_read_b128 v[14:17], v191 offset:1024
	ds_read_b128 v[2:5], v191 offset:2048
	ds_read_b128 v[6:9], v191 offset:3072
	s_add_u32 s28, s26, 0xfffc0080
	s_addc_u32 s29, s27, -1
	s_cmp_eq_u32 s53, 12
	s_cselect_b32 s31, s15, s29
	s_cselect_b32 s30, s49, s28
	s_cselect_b32 s29, s17, s52
	s_cselect_b32 s28, s50, s51
	s_add_i32 m0, s23, 0xc000
	ds_read_b128 v[176:179], v192
	ds_read_b128 v[180:183], v192 offset:1024
	ds_read_b128 v[194:197], v192 offset:2048
	ds_read_b128 v[198:201], v192 offset:3072
	ds_read_b128 v[202:205], v192 offset:4096
	ds_read_b128 v[206:209], v192 offset:5120
	ds_read_b128 v[214:217], v192 offset:6144
	ds_read_b128 v[218:221], v192 offset:7168
	global_load_lds_dwordx4 v170, s[26:27]
	s_add_i32 m0, s23, 0xe000
	s_nop 0
	global_load_lds_dwordx4 v172, s[26:27]
	s_waitcnt vmcnt(8)
	s_waitcnt lgkmcnt(0)
	s_barrier
	s_setprio 1
	s_waitcnt lgkmcnt(0)
	v_mfma_scale_f32_16x16x128_f8f6f4 v[158:161], v[26:33], v[176:183], 0, v1, v184 op_sel_hi:[0,0,0]
	s_add_i32 s43, s43, 1
	s_mul_i32 s0, s43, s44
	s_mul_hi_u32 s1, s43, s82
	s_add_i32 s1, s1, s0
	s_mul_i32 s0, s43, s82
	v_readlane_b32 s15, v247, 6
	v_mfma_scale_f32_16x16x128_f8f6f4 v[154:157], v[18:25], v[176:183], 0, v1, v184 op_sel_hi:[0,0,0]
	s_add_u32 s18, s0, s15
	s_addc_u32 s19, s1, s37
	v_cmp_lt_i64_e64 s[0:1], s[18:19], v[174:175]
	s_ashr_i32 s14, s18, 31
	s_lshr_b32 s14, s14, 29
	s_add_i32 s14, s18, s14
	v_mfma_scale_f32_16x16x128_f8f6f4 v[142:145], v[26:33], v[194:201], 0, v1, v184 op_sel_hi:[0,0,0]
	s_ashr_i32 s15, s14, 3
	s_and_b32 s14, s14, -8
	s_sub_i32 s14, s18, s14
	s_cmp_lt_i32 s14, 0
	s_cselect_b32 s16, s38, s36
	s_mul_i32 s14, s14, s16
	v_mfma_scale_f32_16x16x128_f8f6f4 v[138:141], v[18:25], v[194:201], 0, v1, v184 op_sel_hi:[0,0,0]
	s_add_i32 s14, s14, s15
	s_mul_hi_i32 s15, s14, 0x92492493
	s_add_i32 s15, s15, s14
	s_lshr_b32 s16, s15, 31
	s_ashr_i32 s15, s15, 8
	s_add_i32 s15, s15, s16
	v_mfma_scale_f32_16x16x128_f8f6f4 v[126:129], v[26:33], v[202:209], 0, v1, v184 op_sel_hi:[0,0,0]
	s_lshl_b32 s16, s15, 3
	s_sub_i32 s17, s13, s16
	s_min_i32 s17, s17, 8
	s_abs_i32 s18, s17
	v_cvt_f32_u32_e32 v250, s18
	s_sub_i32 s20, 0, s18
	v_mfma_scale_f32_16x16x128_f8f6f4 v[122:125], v[18:25], v[202:209], 0, v1, v184 op_sel_hi:[0,0,0]
	s_mulk_i32 s15, 0x1c0
	s_sub_i32 s14, s14, s15
	v_rcp_iflag_f32_e32 v250, v250
	s_abs_i32 s15, s14
	s_xor_b32 s19, s14, s17
	s_ashr_i32 s19, s19, 31
	v_mfma_scale_f32_16x16x128_f8f6f4 v[110:113], v[26:33], v[214:221], 0, v1, v184 op_sel_hi:[0,0,0]
	v_mul_f32_e32 v250, 0x4f7ffffe, v250
	v_cvt_u32_f32_e32 v250, v250
	s_nop 0
	v_readfirstlane_b32 s21, v250
	s_mul_i32 s20, s20, s21
	s_mul_hi_u32 s20, s21, s20
	v_mfma_scale_f32_16x16x128_f8f6f4 v[106:109], v[18:25], v[214:221], 0, v1, v184 op_sel_hi:[0,0,0]
	s_add_i32 s21, s21, s20
	s_mul_hi_u32 s20, s15, s21
	s_mul_i32 s21, s20, s18
	s_sub_i32 s15, s15, s21
	s_add_i32 s98, s20, 1
	s_sub_i32 s21, s15, s18
	s_setprio 0
	s_setprio 1
	v_mfma_scale_f32_16x16x128_f8f6f4 v[150:153], v[10:17], v[176:183], 0, v1, v184 op_sel_hi:[0,0,0]
	s_cmp_ge_u32 s15, s18
	s_cselect_b32 s20, s98, s20
	s_cselect_b32 s15, s21, s15
	s_add_i32 s21, s20, 1
	s_cmp_ge_u32 s15, s18
	s_cselect_b32 s15, s21, s20
	v_mfma_scale_f32_16x16x128_f8f6f4 v[146:149], v[2:9], v[176:183], 0, v1, v184 op_sel_hi:[0,0,0]
	s_xor_b32 s15, s15, s19
	s_sub_i32 s15, s15, s19
	s_mul_i32 s17, s15, s17
	s_sub_i32 s14, s14, s17
	s_add_i32 s14, s16, s14
	s_lshl_b32 s16, s14, 2
	v_mfma_scale_f32_16x16x128_f8f6f4 v[134:137], v[10:17], v[194:201], 0, v1, v184 op_sel_hi:[0,0,0]
	s_add_i32 s16, s16, 0
	s_add_i32 s16, s16, 0x20040
	v_mov_b32_e32 v250, s16
	ds_read_b32 v250, v250
	s_waitcnt lgkmcnt(0)
	v_readfirstlane_b32 s16, v250
	v_mfma_scale_f32_16x16x128_f8f6f4 v[130:133], v[2:9], v[194:201], 0, v1, v184 op_sel_hi:[0,0,0]
	s_mul_i32 s16, s16, 56
	s_add_i32 s16, s16, s15
	s_ashr_i32 s15, s14, 31
	s_lshl_b64 s[18:19], s[14:15], 19
	s_add_u32 s18, s8, s18
	s_addc_u32 s19, s9, s19
	v_mfma_scale_f32_16x16x128_f8f6f4 v[118:121], v[10:17], v[202:209], 0, v1, v184 op_sel_hi:[0,0,0]
	s_and_b64 s[20:21], s[0:1], exec
	s_cselect_b32 s15, s19, s27
	s_cselect_b32 s49, s18, s26
	s_ashr_i32 s17, s16, 31
	s_lshl_b64 s[20:21], s[16:17], 19
	s_add_u32 s20, s33, s20
	v_mfma_scale_f32_16x16x128_f8f6f4 v[114:117], v[2:9], v[202:209], 0, v1, v184 op_sel_hi:[0,0,0]
	s_addc_u32 s21, s34, s21
	s_and_b64 s[98:99], s[0:1], exec
	s_cselect_b32 s17, s21, s29
	s_cselect_b32 s50, s20, s28
	v_mfma_scale_f32_16x16x128_f8f6f4 v[102:105], v[10:17], v[214:221], 0, v1, v184 op_sel_hi:[0,0,0]
	v_mfma_scale_f32_16x16x128_f8f6f4 v[98:101], v[2:9], v[214:221], 0, v1, v184 op_sel_hi:[0,0,0]
	s_setprio 0
	s_barrier
	s_add_i32 s54, s45, s35
	s_mov_b32 m0, s54
	ds_read_b128 v[194:197], v192 offset:16384
	ds_read_b128 v[198:201], v192 offset:17408
	ds_read_b128 v[202:205], v192 offset:18432
	ds_read_b128 v[206:209], v192 offset:19456
	ds_read_b128 v[214:217], v192 offset:20480
	ds_read_b128 v[218:221], v192 offset:21504
	ds_read_b128 v[222:225], v192 offset:22528
	ds_read_b128 v[226:229], v192 offset:23552
	global_load_lds_dwordx4 v166, s[28:29]
	s_add_i32 m0, s54, 0x2000
	s_add_u32 s54, s28, 0x40000
	s_addc_u32 s55, s29, 0
	s_add_i32 s56, s46, s35
	global_load_lds_dwordx4 v162, s[28:29]
	s_mov_b32 m0, s56
	s_nop 0
	global_load_lds_dwordx4 v166, s[54:55]
	s_add_i32 m0, s56, 0x2000
	s_nop 0
	global_load_lds_dwordx4 v162, s[54:55]
	s_mov_b32 m0, s23
	s_nop 0
	global_load_lds_dwordx4 v168, s[30:31]
	s_mov_b32 m0, s25
	s_nop 0
	global_load_lds_dwordx4 v164, s[30:31]
	s_waitcnt vmcnt(8)
	s_waitcnt lgkmcnt(0)
	s_barrier
; #define PG8_STAGE(bufoff, gbase, voff) do { _Pragma("unroll") for (int _i = 0; _i < 2; ++_i) \
;         __builtin_amdgcn_global_load_lds((const unsigned*)((const char*)(gbase) + (voff)[_i]), (PG8_LAS unsigned*)(lds + (bufoff) + ldsw + _i * 8192), 16, 0, 0); } while (0)
; #define PG8_LDA(dst, b, h) do { _Pragma("unroll") for (int m = 0; m < 4; ++m) _Pragma("unroll") for (int k = 0; k < 2; ++k) dst[m][k] = *(const PG8_LAS bf16x8*)(lds + PG8_SA(b, h) + aoff + m * 2048 + k * 1024); } while (0)
; #define PG8_LDB(dst, b, h) do { _Pragma("unroll") for (int n = 0; n < 2; ++n) _Pragma("unroll") for (int k = 0; k < 2; ++k) dst[n][k] = *(const PG8_LAS bf16x8*)(lds + PG8_SB(b, h) + boff + n * 2048 + k * 1024); } while (0)
; #define PG8_WAIT_V(n) asm volatile("s_waitcnt vmcnt(" #n ")" ::: "memory")
; #define PG8_WAIT_L(n) asm volatile("s_waitcnt lgkmcnt(" #n ")" ::: "memory")
; #define PG8_BAR __builtin_amdgcn_s_barrier()
; #define PG8_SCHED __builtin_amdgcn_sched_barrier(0)
; template <class Epi, class Sched, bool ALIGN_EPI = false, bool SP2 = false>
; __device__ __forceinline__ void gemm_phase(PG8_LAS unsigned char* lds, const Gemm g, const Sched& S, const Epi& E) {
;     ...
;             PG8_WAIT_V(8); PG8_WAIT_L(0); PG8_BAR; PG8_MMA(1, 0, At, B0); PG8_MMA(1, 1, At, B1); PG8_BAR; PG8_SCHED;
;             PG8_LDB(B0, 1, 0); PG8_LDB(B1, 1, 1); PG8_SCHED; PG8_LDA(At, 1, 0); PG8_STAGE(PG8_SA(0, 1), a2 + hstep, voffA);
;             PG8_WAIT_V(8); PG8_WAIT_L(0); PG8_BAR; PG8_MMA(0, 0, At, B0); PG8_MMA(0, 1, At, B1); PG8_BAR; PG8_SCHED;
	s_setprio 1
	s_waitcnt lgkmcnt(0)
	v_mfma_scale_f32_16x16x128_f8f6f4 v[94:97], v[26:33], v[194:201], 0, v1, v184 op_sel_hi:[0,0,0]
	v_mfma_scale_f32_16x16x128_f8f6f4 v[90:93], v[18:25], v[194:201], 0, v1, v184 op_sel_hi:[0,0,0]
	v_mfma_scale_f32_16x16x128_f8f6f4 v[78:81], v[26:33], v[202:209], 0, v1, v184 op_sel_hi:[0,0,0]
	v_mfma_scale_f32_16x16x128_f8f6f4 v[74:77], v[18:25], v[202:209], 0, v1, v184 op_sel_hi:[0,0,0]
	v_mfma_scale_f32_16x16x128_f8f6f4 v[62:65], v[26:33], v[214:221], 0, v1, v184 op_sel_hi:[0,0,0]
	v_mfma_scale_f32_16x16x128_f8f6f4 v[58:61], v[18:25], v[214:221], 0, v1, v184 op_sel_hi:[0,0,0]
	v_mfma_scale_f32_16x16x128_f8f6f4 v[46:49], v[26:33], v[222:229], 0, v1, v184 op_sel_hi:[0,0,0]
	v_mfma_scale_f32_16x16x128_f8f6f4 v[42:45], v[18:25], v[222:229], 0, v1, v184 op_sel_hi:[0,0,0]
	s_setprio 0
	s_setprio 1
	v_mfma_scale_f32_16x16x128_f8f6f4 v[86:89], v[10:17], v[194:201], 0, v1, v184 op_sel_hi:[0,0,0]
	v_mfma_scale_f32_16x16x128_f8f6f4 v[82:85], v[2:9], v[194:201], 0, v1, v184 op_sel_hi:[0,0,0]
	v_mfma_scale_f32_16x16x128_f8f6f4 v[70:73], v[10:17], v[202:209], 0, v1, v184 op_sel_hi:[0,0,0]
	v_mfma_scale_f32_16x16x128_f8f6f4 v[66:69], v[2:9], v[202:209], 0, v1, v184 op_sel_hi:[0,0,0]
	v_mfma_scale_f32_16x16x128_f8f6f4 v[54:57], v[10:17], v[214:221], 0, v1, v184 op_sel_hi:[0,0,0]
	v_mfma_scale_f32_16x16x128_f8f6f4 v[50:53], v[2:9], v[214:221], 0, v1, v184 op_sel_hi:[0,0,0]
	v_mfma_scale_f32_16x16x128_f8f6f4 v[38:41], v[10:17], v[222:229], 0, v1, v184 op_sel_hi:[0,0,0]
	v_mfma_scale_f32_16x16x128_f8f6f4 v[34:37], v[2:9], v[222:229], 0, v1, v184 op_sel_hi:[0,0,0]
	s_setprio 0
	s_barrier
	s_add_i32 s54, 0, 0x18000
	s_add_i32 s55, 0, 0x1c000
	ds_read_b128 v[2:5], v248
	ds_read_b128 v[6:9], v248 offset:1024
	ds_read_b128 v[10:13], v248 offset:2048
	ds_read_b128 v[14:17], v248 offset:3072
	ds_read_b128 v[18:21], v249
	ds_read_b128 v[22:25], v249 offset:1024
	ds_read_b128 v[26:29], v249 offset:2048
	ds_read_b128 v[30:33], v249 offset:3072
	s_add_u32 s30, s30, 0x40000
	s_addc_u32 s31, s31, 0
	s_mov_b32 m0, s39
	ds_read_b128 v[194:197], v192 offset:32768
	ds_read_b128 v[198:201], v192 offset:33792
	ds_read_b128 v[202:205], v192 offset:34816
	ds_read_b128 v[206:209], v192 offset:35840
	ds_read_b128 v[214:217], v192 offset:36864
	ds_read_b128 v[218:221], v192 offset:37888
	ds_read_b128 v[222:225], v192 offset:38912
	ds_read_b128 v[226:229], v192 offset:39936
	global_load_lds_dwordx4 v168, s[30:31]
	s_mov_b32 m0, s40
	s_nop 0
	global_load_lds_dwordx4 v164, s[30:31]
	s_waitcnt vmcnt(8)
	s_waitcnt lgkmcnt(0)
	s_barrier
	s_setprio 1
	s_waitcnt lgkmcnt(0)
	v_mfma_scale_f32_16x16x128_f8f6f4 v[158:161], v[2:9], v[194:201], v[158:161], v1, v184 op_sel_hi:[0,0,0]
	v_mfma_scale_f32_16x16x128_f8f6f4 v[154:157], v[10:17], v[194:201], v[154:157], v1, v184 op_sel_hi:[0,0,0]
	v_mfma_scale_f32_16x16x128_f8f6f4 v[142:145], v[2:9], v[202:209], v[142:145], v1, v184 op_sel_hi:[0,0,0]
	v_mfma_scale_f32_16x16x128_f8f6f4 v[138:141], v[10:17], v[202:209], v[138:141], v1, v184 op_sel_hi:[0,0,0]
	v_mfma_scale_f32_16x16x128_f8f6f4 v[126:129], v[2:9], v[214:221], v[126:129], v1, v184 op_sel_hi:[0,0,0]
	v_mfma_scale_f32_16x16x128_f8f6f4 v[122:125], v[10:17], v[214:221], v[122:125], v1, v184 op_sel_hi:[0,0,0]
	v_mfma_scale_f32_16x16x128_f8f6f4 v[110:113], v[2:9], v[222:229], v[110:113], v1, v184 op_sel_hi:[0,0,0]
	v_mfma_scale_f32_16x16x128_f8f6f4 v[106:109], v[10:17], v[222:229], v[106:109], v1, v184 op_sel_hi:[0,0,0]
	s_setprio 0
	s_setprio 1
	v_mfma_scale_f32_16x16x128_f8f6f4 v[150:153], v[18:25], v[194:201], v[150:153], v1, v184 op_sel_hi:[0,0,0]
	v_mfma_scale_f32_16x16x128_f8f6f4 v[146:149], v[26:33], v[194:201], v[146:149], v1, v184 op_sel_hi:[0,0,0]
	v_mfma_scale_f32_16x16x128_f8f6f4 v[134:137], v[18:25], v[202:209], v[134:137], v1, v184 op_sel_hi:[0,0,0]
	v_mfma_scale_f32_16x16x128_f8f6f4 v[130:133], v[26:33], v[202:209], v[130:133], v1, v184 op_sel_hi:[0,0,0]
	v_mfma_scale_f32_16x16x128_f8f6f4 v[118:121], v[18:25], v[214:221], v[118:121], v1, v184 op_sel_hi:[0,0,0]
	v_mfma_scale_f32_16x16x128_f8f6f4 v[114:117], v[26:33], v[214:221], v[114:117], v1, v184 op_sel_hi:[0,0,0]
	v_mfma_scale_f32_16x16x128_f8f6f4 v[102:105], v[18:25], v[222:229], v[102:105], v1, v184 op_sel_hi:[0,0,0]
	v_mfma_scale_f32_16x16x128_f8f6f4 v[98:101], v[26:33], v[222:229], v[98:101], v1, v184 op_sel_hi:[0,0,0]
	s_setprio 0
	s_barrier
; #define PG8_STAGE(bufoff, gbase, voff) do { _Pragma("unroll") for (int _i = 0; _i < 2; ++_i) \
;         __builtin_amdgcn_global_load_lds((const unsigned*)((const char*)(gbase) + (voff)[_i]), (PG8_LAS unsigned*)(lds + (bufoff) + ldsw + _i * 8192), 16, 0, 0); } while (0)
; #define PG8_LDA(dst, b, h) do { _Pragma("unroll") for (int m = 0; m < 4; ++m) _Pragma("unroll") for (int k = 0; k < 2; ++k) dst[m][k] = *(const PG8_LAS bf16x8*)(lds + PG8_SA(b, h) + aoff + m * 2048 + k * 1024); } while (0)
; #define PG8_WAIT_V(n) asm volatile("s_waitcnt vmcnt(" #n ")" ::: "memory")
; #define PG8_WAIT_L(n) asm volatile("s_waitcnt lgkmcnt(" #n ")" ::: "memory")
; #define PG8_BAR __builtin_amdgcn_s_barrier()
; #define PG8_SCHED __builtin_amdgcn_sched_barrier(0)
; template <class Epi, class Sched, bool ALIGN_EPI = false, bool SP2 = false>
; __device__ __forceinline__ void gemm_phase(PG8_LAS unsigned char* lds, const Gemm g, const Sched& S, const Epi& E) {
;     ...
;             PG8_LDA(At, 1, 1); PG8_STAGE(PG8_SB(1, 0), b3, voffB); PG8_STAGE(PG8_SB(1, 1), b3 + hstep, voffB); PG8_STAGE(PG8_SA(1, 0), a3, voffA);
;             PG8_WAIT_V(8); PG8_WAIT_L(0); PG8_BAR; PG8_MMA(1, 0, At, B0); PG8_MMA(1, 1, At, B1); PG8_BAR; PG8_SCHED;
	s_add_u32 s98, s28, 0x80
	s_addc_u32 s99, s29, 0
	s_add_u32 s100, s30, 0xfffc0080
	s_addc_u32 s101, s31, -1
	s_add_i32 s30, s54, s35
	s_mov_b32 m0, s30
	ds_read_b128 v[194:197], v192 offset:49152
	ds_read_b128 v[198:201], v192 offset:50176
	ds_read_b128 v[202:205], v192 offset:51200
	ds_read_b128 v[206:209], v192 offset:52224
	ds_read_b128 v[214:217], v192 offset:53248
	ds_read_b128 v[218:221], v192 offset:54272
	ds_read_b128 v[222:225], v192 offset:55296
	ds_read_b128 v[226:229], v192 offset:56320
	global_load_lds_dwordx4 v166, s[98:99]
	s_add_i32 m0, s30, 0x2000
	s_add_u32 s28, s28, 0x40080
	s_addc_u32 s29, s29, 0
	s_add_i32 s30, s55, s35
	global_load_lds_dwordx4 v162, s[98:99]
	s_mov_b32 m0, s30
	s_nop 0
	global_load_lds_dwordx4 v166, s[28:29]
	s_add_i32 m0, s30, 0x2000
	s_nop 0
	global_load_lds_dwordx4 v162, s[28:29]
	s_mov_b32 m0, s41
	s_nop 0
	global_load_lds_dwordx4 v168, s[100:101]
	s_mov_b32 m0, s42
	s_nop 0
	global_load_lds_dwordx4 v164, s[100:101]
	s_waitcnt vmcnt(8)
	s_waitcnt lgkmcnt(0)
	s_barrier
	s_setprio 1
	s_waitcnt lgkmcnt(0)
	v_mfma_scale_f32_16x16x128_f8f6f4 v[94:97], v[2:9], v[194:201], v[94:97], v1, v184 op_sel_hi:[0,0,0]
	v_mfma_scale_f32_16x16x128_f8f6f4 v[90:93], v[10:17], v[194:201], v[90:93], v1, v184 op_sel_hi:[0,0,0]
	v_mfma_scale_f32_16x16x128_f8f6f4 v[78:81], v[2:9], v[202:209], v[78:81], v1, v184 op_sel_hi:[0,0,0]
	v_mfma_scale_f32_16x16x128_f8f6f4 v[74:77], v[10:17], v[202:209], v[74:77], v1, v184 op_sel_hi:[0,0,0]
	v_mfma_scale_f32_16x16x128_f8f6f4 v[62:65], v[2:9], v[214:221], v[62:65], v1, v184 op_sel_hi:[0,0,0]
	v_mfma_scale_f32_16x16x128_f8f6f4 v[58:61], v[10:17], v[214:221], v[58:61], v1, v184 op_sel_hi:[0,0,0]
	v_mfma_scale_f32_16x16x128_f8f6f4 v[46:49], v[2:9], v[222:229], v[46:49], v1, v184 op_sel_hi:[0,0,0]
	v_mfma_scale_f32_16x16x128_f8f6f4 v[42:45], v[10:17], v[222:229], v[42:45], v1, v184 op_sel_hi:[0,0,0]
	s_setprio 0
	s_setprio 1
	v_mfma_scale_f32_16x16x128_f8f6f4 v[86:89], v[18:25], v[194:201], v[86:89], v1, v184 op_sel_hi:[0,0,0]
	v_mfma_scale_f32_16x16x128_f8f6f4 v[82:85], v[26:33], v[194:201], v[82:85], v1, v184 op_sel_hi:[0,0,0]
	v_mfma_scale_f32_16x16x128_f8f6f4 v[70:73], v[18:25], v[202:209], v[70:73], v1, v184 op_sel_hi:[0,0,0]
	v_mfma_scale_f32_16x16x128_f8f6f4 v[66:69], v[26:33], v[202:209], v[66:69], v1, v184 op_sel_hi:[0,0,0]
	v_mfma_scale_f32_16x16x128_f8f6f4 v[54:57], v[18:25], v[214:221], v[54:57], v1, v184 op_sel_hi:[0,0,0]
	v_mfma_scale_f32_16x16x128_f8f6f4 v[50:53], v[26:33], v[214:221], v[50:53], v1, v184 op_sel_hi:[0,0,0]
	v_mfma_scale_f32_16x16x128_f8f6f4 v[38:41], v[18:25], v[222:229], v[38:41], v1, v184 op_sel_hi:[0,0,0]
	v_mfma_scale_f32_16x16x128_f8f6f4 v[34:37], v[26:33], v[222:229], v[34:37], v1, v184 op_sel_hi:[0,0,0]
	s_setprio 0
	s_barrier
	s_add_i32 s53, s53, 2
	s_add_u32 s26, s26, 0x100
	s_addc_u32 s27, s27, 0
	s_add_u32 s51, s51, 0x100
	s_addc_u32 s52, s52, 0
	s_cmp_gt_u32 s53, 13
